# speedup vs baseline: 1.0156x; 1.0156x over previous
_Z11prep_kernelPKfS0_S0_PDF16_PfPiS0_S1_:
	s_cmpk_lt_u32 s2, 0xc1
	s_mov_b64 s[4:5], -1
	s_cbranch_scc0 .LBB0_51
	s_cmpk_lg_i32 s2, 0xc0
	s_cbranch_scc0 .LBB0_11
	s_cmp_gt_u32 s2, 63
	s_cbranch_scc0 .LBB0_8
	s_load_dwordx4 s[4:7], s[0:1], 0x0
	s_lshl_b32 s3, s2, 2
	s_addk_i32 s3, 0xff00
	v_readfirstlane_b32 s23, v0
	v_lshlrev_b32_e32 v1, 2, v0
	v_and_b32_e32 v1, 0x1fc, v1
	v_lshlrev_b32_e32 v26, 2, v1
	v_mov_b32_e32 v27, 0
	s_lshr_b32 s22, s23, 7
	s_lshl_b32 s8, s3, 9
	s_lshl_b32 s9, s22, 7
	s_add_u32 s8, s8, s9
	s_lshl_b32 s10, s22, 16
	s_waitcnt lgkmcnt(0)
	s_add_u32 s20, s4, s8
	s_addc_u32 s21, s5, 0
	s_add_u32 s24, s6, s10
	s_addc_u32 s25, s7, 0
	global_load_dwordx4 v[32:35], v26, s[24:25]
	global_load_dwordx4 v[36:39], v26, s[24:25] offset:2048
	s_add_u32 s24, s24, 0x1000
	s_addc_u32 s25, s25, 0
	s_load_dwordx8 s[32:39], s[20:21], 0x0
	s_load_dwordx8 s[40:47], s[20:21], 0x200
	s_load_dwordx8 s[48:55], s[20:21], 0x400
	s_load_dwordx8 s[56:63], s[20:21], 0x600
	global_load_dwordx4 v[40:43], v26, s[24:25]
	global_load_dwordx4 v[44:47], v26, s[24:25] offset:2048
	s_add_u32 s24, s24, 0x1000
	s_addc_u32 s25, s25, 0
	s_load_dwordx8 s[64:71], s[20:21], 0x20
	s_load_dwordx8 s[72:79], s[20:21], 0x220
	s_load_dwordx8 s[80:87], s[20:21], 0x420
	s_load_dwordx8 s[88:95], s[20:21], 0x620
	global_load_dwordx4 v[48:51], v26, s[24:25]
	global_load_dwordx4 v[52:55], v26, s[24:25] offset:2048
	s_add_u32 s24, s24, 0x1000
	s_addc_u32 s25, s25, 0
	global_load_dwordx4 v[56:59], v26, s[24:25]
	global_load_dwordx4 v[60:63], v26, s[24:25] offset:2048
	s_add_u32 s24, s24, 0x1000
	s_addc_u32 s25, s25, 0
	global_load_dwordx4 v[64:67], v26, s[24:25]
	global_load_dwordx4 v[68:71], v26, s[24:25] offset:2048
	s_add_u32 s24, s24, 0x1000
	s_addc_u32 s25, s25, 0
	global_load_dwordx4 v[72:75], v26, s[24:25]
	global_load_dwordx4 v[76:79], v26, s[24:25] offset:2048
	s_add_u32 s24, s24, 0x1000
	s_addc_u32 s25, s25, 0
	global_load_dwordx4 v[80:83], v26, s[24:25]
	global_load_dwordx4 v[84:87], v26, s[24:25] offset:2048
	s_add_u32 s24, s24, 0x1000
	s_addc_u32 s25, s25, 0
	global_load_dwordx4 v[88:91], v26, s[24:25]
	global_load_dwordx4 v[92:95], v26, s[24:25] offset:2048
	s_add_u32 s24, s24, 0x1000
	s_addc_u32 s25, s25, 0
	global_load_dwordx4 v[96:99], v26, s[24:25]
	global_load_dwordx4 v[100:103], v26, s[24:25] offset:2048
	s_add_u32 s24, s24, 0x1000
	s_addc_u32 s25, s25, 0
	global_load_dwordx4 v[104:107], v26, s[24:25]
	global_load_dwordx4 v[108:111], v26, s[24:25] offset:2048
	s_add_u32 s24, s24, 0x1000
	s_addc_u32 s25, s25, 0
	global_load_dwordx4 v[112:115], v26, s[24:25]
	global_load_dwordx4 v[116:119], v26, s[24:25] offset:2048
	s_add_u32 s24, s24, 0x1000
	s_addc_u32 s25, s25, 0
	global_load_dwordx4 v[120:123], v26, s[24:25]
	global_load_dwordx4 v[124:127], v26, s[24:25] offset:2048
	s_add_u32 s24, s24, 0x1000
	s_addc_u32 s25, s25, 0
	global_load_dwordx4 v[128:131], v26, s[24:25]
	global_load_dwordx4 v[132:135], v26, s[24:25] offset:2048
	s_add_u32 s24, s24, 0x1000
	s_addc_u32 s25, s25, 0
	global_load_dwordx4 v[136:139], v26, s[24:25]
	global_load_dwordx4 v[140:143], v26, s[24:25] offset:2048
	s_add_u32 s24, s24, 0x1000
	s_addc_u32 s25, s25, 0
	global_load_dwordx4 v[144:147], v26, s[24:25]
	global_load_dwordx4 v[148:151], v26, s[24:25] offset:2048
	s_add_u32 s24, s24, 0x1000
	s_addc_u32 s25, s25, 0
	global_load_dwordx4 v[152:155], v26, s[24:25]
	global_load_dwordx4 v[156:159], v26, s[24:25] offset:2048
	v_mov_b64_e32 v[14:15], 0
	v_mov_b64_e32 v[16:17], 0
	v_mov_b64_e32 v[10:11], 0
	v_mov_b64_e32 v[12:13], 0
	v_mov_b64_e32 v[6:7], 0
	v_mov_b64_e32 v[8:9], 0
	v_mov_b64_e32 v[2:3], 0
	v_mov_b64_e32 v[4:5], 0
	s_waitcnt lgkmcnt(0)
	s_waitcnt vmcnt(31)
	v_pk_fma_f32 v[14:15], s[32:33], v[32:33], v[14:15] op_sel_hi:[0,1,1]
	v_pk_fma_f32 v[16:17], s[32:33], v[34:35], v[16:17] op_sel_hi:[0,1,1]
	v_pk_fma_f32 v[10:11], s[40:41], v[32:33], v[10:11] op_sel_hi:[0,1,1]
	v_pk_fma_f32 v[12:13], s[40:41], v[34:35], v[12:13] op_sel_hi:[0,1,1]
	v_pk_fma_f32 v[6:7], s[48:49], v[32:33], v[6:7] op_sel_hi:[0,1,1]
	v_pk_fma_f32 v[8:9], s[48:49], v[34:35], v[8:9] op_sel_hi:[0,1,1]
	v_pk_fma_f32 v[2:3], s[56:57], v[32:33], v[2:3] op_sel_hi:[0,1,1]
	v_pk_fma_f32 v[4:5], s[56:57], v[34:35], v[4:5] op_sel_hi:[0,1,1]
	s_waitcnt vmcnt(30)
	v_pk_fma_f32 v[14:15], s[32:33], v[36:37], v[14:15] op_sel:[1,0,0]
	v_pk_fma_f32 v[16:17], s[32:33], v[38:39], v[16:17] op_sel:[1,0,0]
	v_pk_fma_f32 v[10:11], s[40:41], v[36:37], v[10:11] op_sel:[1,0,0]
	v_pk_fma_f32 v[12:13], s[40:41], v[38:39], v[12:13] op_sel:[1,0,0]
	v_pk_fma_f32 v[6:7], s[48:49], v[36:37], v[6:7] op_sel:[1,0,0]
	v_pk_fma_f32 v[8:9], s[48:49], v[38:39], v[8:9] op_sel:[1,0,0]
	v_pk_fma_f32 v[2:3], s[56:57], v[36:37], v[2:3] op_sel:[1,0,0]
	v_pk_fma_f32 v[4:5], s[56:57], v[38:39], v[4:5] op_sel:[1,0,0]
	s_waitcnt vmcnt(29)
	v_pk_fma_f32 v[14:15], s[34:35], v[40:41], v[14:15] op_sel_hi:[0,1,1]
	v_pk_fma_f32 v[16:17], s[34:35], v[42:43], v[16:17] op_sel_hi:[0,1,1]
	v_pk_fma_f32 v[10:11], s[42:43], v[40:41], v[10:11] op_sel_hi:[0,1,1]
	v_pk_fma_f32 v[12:13], s[42:43], v[42:43], v[12:13] op_sel_hi:[0,1,1]
	v_pk_fma_f32 v[6:7], s[50:51], v[40:41], v[6:7] op_sel_hi:[0,1,1]
	v_pk_fma_f32 v[8:9], s[50:51], v[42:43], v[8:9] op_sel_hi:[0,1,1]
	v_pk_fma_f32 v[2:3], s[58:59], v[40:41], v[2:3] op_sel_hi:[0,1,1]
	v_pk_fma_f32 v[4:5], s[58:59], v[42:43], v[4:5] op_sel_hi:[0,1,1]
	s_waitcnt vmcnt(28)
	v_pk_fma_f32 v[14:15], s[34:35], v[44:45], v[14:15] op_sel:[1,0,0]
	v_pk_fma_f32 v[16:17], s[34:35], v[46:47], v[16:17] op_sel:[1,0,0]
	v_pk_fma_f32 v[10:11], s[42:43], v[44:45], v[10:11] op_sel:[1,0,0]
	v_pk_fma_f32 v[12:13], s[42:43], v[46:47], v[12:13] op_sel:[1,0,0]
	v_pk_fma_f32 v[6:7], s[50:51], v[44:45], v[6:7] op_sel:[1,0,0]
	v_pk_fma_f32 v[8:9], s[50:51], v[46:47], v[8:9] op_sel:[1,0,0]
	v_pk_fma_f32 v[2:3], s[58:59], v[44:45], v[2:3] op_sel:[1,0,0]
	v_pk_fma_f32 v[4:5], s[58:59], v[46:47], v[4:5] op_sel:[1,0,0]
	s_waitcnt vmcnt(27)
	v_pk_fma_f32 v[14:15], s[36:37], v[48:49], v[14:15] op_sel_hi:[0,1,1]
	v_pk_fma_f32 v[16:17], s[36:37], v[50:51], v[16:17] op_sel_hi:[0,1,1]
	v_pk_fma_f32 v[10:11], s[44:45], v[48:49], v[10:11] op_sel_hi:[0,1,1]
	v_pk_fma_f32 v[12:13], s[44:45], v[50:51], v[12:13] op_sel_hi:[0,1,1]
	v_pk_fma_f32 v[6:7], s[52:53], v[48:49], v[6:7] op_sel_hi:[0,1,1]
	v_pk_fma_f32 v[8:9], s[52:53], v[50:51], v[8:9] op_sel_hi:[0,1,1]
	v_pk_fma_f32 v[2:3], s[60:61], v[48:49], v[2:3] op_sel_hi:[0,1,1]
	v_pk_fma_f32 v[4:5], s[60:61], v[50:51], v[4:5] op_sel_hi:[0,1,1]
	s_waitcnt vmcnt(26)
	v_pk_fma_f32 v[14:15], s[36:37], v[52:53], v[14:15] op_sel:[1,0,0]
	v_pk_fma_f32 v[16:17], s[36:37], v[54:55], v[16:17] op_sel:[1,0,0]
	v_pk_fma_f32 v[10:11], s[44:45], v[52:53], v[10:11] op_sel:[1,0,0]
	v_pk_fma_f32 v[12:13], s[44:45], v[54:55], v[12:13] op_sel:[1,0,0]
	v_pk_fma_f32 v[6:7], s[52:53], v[52:53], v[6:7] op_sel:[1,0,0]
	v_pk_fma_f32 v[8:9], s[52:53], v[54:55], v[8:9] op_sel:[1,0,0]
	v_pk_fma_f32 v[2:3], s[60:61], v[52:53], v[2:3] op_sel:[1,0,0]
	v_pk_fma_f32 v[4:5], s[60:61], v[54:55], v[4:5] op_sel:[1,0,0]
	s_waitcnt vmcnt(25)
	v_pk_fma_f32 v[14:15], s[38:39], v[56:57], v[14:15] op_sel_hi:[0,1,1]
	v_pk_fma_f32 v[16:17], s[38:39], v[58:59], v[16:17] op_sel_hi:[0,1,1]
	v_pk_fma_f32 v[10:11], s[46:47], v[56:57], v[10:11] op_sel_hi:[0,1,1]
	v_pk_fma_f32 v[12:13], s[46:47], v[58:59], v[12:13] op_sel_hi:[0,1,1]
	v_pk_fma_f32 v[6:7], s[54:55], v[56:57], v[6:7] op_sel_hi:[0,1,1]
	v_pk_fma_f32 v[8:9], s[54:55], v[58:59], v[8:9] op_sel_hi:[0,1,1]
	v_pk_fma_f32 v[2:3], s[62:63], v[56:57], v[2:3] op_sel_hi:[0,1,1]
	v_pk_fma_f32 v[4:5], s[62:63], v[58:59], v[4:5] op_sel_hi:[0,1,1]
	s_waitcnt vmcnt(24)
	v_pk_fma_f32 v[14:15], s[38:39], v[60:61], v[14:15] op_sel:[1,0,0]
	v_pk_fma_f32 v[16:17], s[38:39], v[62:63], v[16:17] op_sel:[1,0,0]
	v_pk_fma_f32 v[10:11], s[46:47], v[60:61], v[10:11] op_sel:[1,0,0]
	v_pk_fma_f32 v[12:13], s[46:47], v[62:63], v[12:13] op_sel:[1,0,0]
	v_pk_fma_f32 v[6:7], s[54:55], v[60:61], v[6:7] op_sel:[1,0,0]
	v_pk_fma_f32 v[8:9], s[54:55], v[62:63], v[8:9] op_sel:[1,0,0]
	v_pk_fma_f32 v[2:3], s[62:63], v[60:61], v[2:3] op_sel:[1,0,0]
	v_pk_fma_f32 v[4:5], s[62:63], v[62:63], v[4:5] op_sel:[1,0,0]
	s_load_dwordx8 s[32:39], s[20:21], 0x40
	s_load_dwordx8 s[40:47], s[20:21], 0x240
	s_load_dwordx8 s[48:55], s[20:21], 0x440
	s_load_dwordx8 s[56:63], s[20:21], 0x640
	s_waitcnt vmcnt(23)
	v_pk_fma_f32 v[14:15], s[64:65], v[64:65], v[14:15] op_sel_hi:[0,1,1]
	v_pk_fma_f32 v[16:17], s[64:65], v[66:67], v[16:17] op_sel_hi:[0,1,1]
	v_pk_fma_f32 v[10:11], s[72:73], v[64:65], v[10:11] op_sel_hi:[0,1,1]
	v_pk_fma_f32 v[12:13], s[72:73], v[66:67], v[12:13] op_sel_hi:[0,1,1]
	v_pk_fma_f32 v[6:7], s[80:81], v[64:65], v[6:7] op_sel_hi:[0,1,1]
	v_pk_fma_f32 v[8:9], s[80:81], v[66:67], v[8:9] op_sel_hi:[0,1,1]
	v_pk_fma_f32 v[2:3], s[88:89], v[64:65], v[2:3] op_sel_hi:[0,1,1]
	v_pk_fma_f32 v[4:5], s[88:89], v[66:67], v[4:5] op_sel_hi:[0,1,1]
	s_waitcnt vmcnt(22)
	v_pk_fma_f32 v[14:15], s[64:65], v[68:69], v[14:15] op_sel:[1,0,0]
	v_pk_fma_f32 v[16:17], s[64:65], v[70:71], v[16:17] op_sel:[1,0,0]
	v_pk_fma_f32 v[10:11], s[72:73], v[68:69], v[10:11] op_sel:[1,0,0]
	v_pk_fma_f32 v[12:13], s[72:73], v[70:71], v[12:13] op_sel:[1,0,0]
	v_pk_fma_f32 v[6:7], s[80:81], v[68:69], v[6:7] op_sel:[1,0,0]
	v_pk_fma_f32 v[8:9], s[80:81], v[70:71], v[8:9] op_sel:[1,0,0]
	v_pk_fma_f32 v[2:3], s[88:89], v[68:69], v[2:3] op_sel:[1,0,0]
	v_pk_fma_f32 v[4:5], s[88:89], v[70:71], v[4:5] op_sel:[1,0,0]
	s_waitcnt vmcnt(21)
	v_pk_fma_f32 v[14:15], s[66:67], v[72:73], v[14:15] op_sel_hi:[0,1,1]
	v_pk_fma_f32 v[16:17], s[66:67], v[74:75], v[16:17] op_sel_hi:[0,1,1]
	v_pk_fma_f32 v[10:11], s[74:75], v[72:73], v[10:11] op_sel_hi:[0,1,1]
	v_pk_fma_f32 v[12:13], s[74:75], v[74:75], v[12:13] op_sel_hi:[0,1,1]
	v_pk_fma_f32 v[6:7], s[82:83], v[72:73], v[6:7] op_sel_hi:[0,1,1]
	v_pk_fma_f32 v[8:9], s[82:83], v[74:75], v[8:9] op_sel_hi:[0,1,1]
	v_pk_fma_f32 v[2:3], s[90:91], v[72:73], v[2:3] op_sel_hi:[0,1,1]
	v_pk_fma_f32 v[4:5], s[90:91], v[74:75], v[4:5] op_sel_hi:[0,1,1]
	s_waitcnt vmcnt(20)
	v_pk_fma_f32 v[14:15], s[66:67], v[76:77], v[14:15] op_sel:[1,0,0]
	v_pk_fma_f32 v[16:17], s[66:67], v[78:79], v[16:17] op_sel:[1,0,0]
	v_pk_fma_f32 v[10:11], s[74:75], v[76:77], v[10:11] op_sel:[1,0,0]
	v_pk_fma_f32 v[12:13], s[74:75], v[78:79], v[12:13] op_sel:[1,0,0]
	v_pk_fma_f32 v[6:7], s[82:83], v[76:77], v[6:7] op_sel:[1,0,0]
	v_pk_fma_f32 v[8:9], s[82:83], v[78:79], v[8:9] op_sel:[1,0,0]
	v_pk_fma_f32 v[2:3], s[90:91], v[76:77], v[2:3] op_sel:[1,0,0]
	v_pk_fma_f32 v[4:5], s[90:91], v[78:79], v[4:5] op_sel:[1,0,0]
	s_waitcnt vmcnt(19)
	v_pk_fma_f32 v[14:15], s[68:69], v[80:81], v[14:15] op_sel_hi:[0,1,1]
	v_pk_fma_f32 v[16:17], s[68:69], v[82:83], v[16:17] op_sel_hi:[0,1,1]
	v_pk_fma_f32 v[10:11], s[76:77], v[80:81], v[10:11] op_sel_hi:[0,1,1]
	v_pk_fma_f32 v[12:13], s[76:77], v[82:83], v[12:13] op_sel_hi:[0,1,1]
	v_pk_fma_f32 v[6:7], s[84:85], v[80:81], v[6:7] op_sel_hi:[0,1,1]
	v_pk_fma_f32 v[8:9], s[84:85], v[82:83], v[8:9] op_sel_hi:[0,1,1]
	v_pk_fma_f32 v[2:3], s[92:93], v[80:81], v[2:3] op_sel_hi:[0,1,1]
	v_pk_fma_f32 v[4:5], s[92:93], v[82:83], v[4:5] op_sel_hi:[0,1,1]
	s_waitcnt vmcnt(18)
	v_pk_fma_f32 v[14:15], s[68:69], v[84:85], v[14:15] op_sel:[1,0,0]
	v_pk_fma_f32 v[16:17], s[68:69], v[86:87], v[16:17] op_sel:[1,0,0]
	v_pk_fma_f32 v[10:11], s[76:77], v[84:85], v[10:11] op_sel:[1,0,0]
	v_pk_fma_f32 v[12:13], s[76:77], v[86:87], v[12:13] op_sel:[1,0,0]
	v_pk_fma_f32 v[6:7], s[84:85], v[84:85], v[6:7] op_sel:[1,0,0]
	v_pk_fma_f32 v[8:9], s[84:85], v[86:87], v[8:9] op_sel:[1,0,0]
	v_pk_fma_f32 v[2:3], s[92:93], v[84:85], v[2:3] op_sel:[1,0,0]
	v_pk_fma_f32 v[4:5], s[92:93], v[86:87], v[4:5] op_sel:[1,0,0]
	s_waitcnt vmcnt(17)
	v_pk_fma_f32 v[14:15], s[70:71], v[88:89], v[14:15] op_sel_hi:[0,1,1]
	v_pk_fma_f32 v[16:17], s[70:71], v[90:91], v[16:17] op_sel_hi:[0,1,1]
	v_pk_fma_f32 v[10:11], s[78:79], v[88:89], v[10:11] op_sel_hi:[0,1,1]
	v_pk_fma_f32 v[12:13], s[78:79], v[90:91], v[12:13] op_sel_hi:[0,1,1]
	v_pk_fma_f32 v[6:7], s[86:87], v[88:89], v[6:7] op_sel_hi:[0,1,1]
	v_pk_fma_f32 v[8:9], s[86:87], v[90:91], v[8:9] op_sel_hi:[0,1,1]
	v_pk_fma_f32 v[2:3], s[94:95], v[88:89], v[2:3] op_sel_hi:[0,1,1]
	v_pk_fma_f32 v[4:5], s[94:95], v[90:91], v[4:5] op_sel_hi:[0,1,1]
	s_waitcnt vmcnt(16)
	v_pk_fma_f32 v[14:15], s[70:71], v[92:93], v[14:15] op_sel:[1,0,0]
	v_pk_fma_f32 v[16:17], s[70:71], v[94:95], v[16:17] op_sel:[1,0,0]
	v_pk_fma_f32 v[10:11], s[78:79], v[92:93], v[10:11] op_sel:[1,0,0]
	v_pk_fma_f32 v[12:13], s[78:79], v[94:95], v[12:13] op_sel:[1,0,0]
	v_pk_fma_f32 v[6:7], s[86:87], v[92:93], v[6:7] op_sel:[1,0,0]
	v_pk_fma_f32 v[8:9], s[86:87], v[94:95], v[8:9] op_sel:[1,0,0]
	v_pk_fma_f32 v[2:3], s[94:95], v[92:93], v[2:3] op_sel:[1,0,0]
	v_pk_fma_f32 v[4:5], s[94:95], v[94:95], v[4:5] op_sel:[1,0,0]
	s_waitcnt lgkmcnt(0)
	s_load_dwordx8 s[64:71], s[20:21], 0x60
	s_load_dwordx8 s[72:79], s[20:21], 0x260
	s_load_dwordx8 s[80:87], s[20:21], 0x460
	s_load_dwordx8 s[88:95], s[20:21], 0x660
	s_waitcnt vmcnt(15)
	v_pk_fma_f32 v[14:15], s[32:33], v[96:97], v[14:15] op_sel_hi:[0,1,1]
	v_pk_fma_f32 v[16:17], s[32:33], v[98:99], v[16:17] op_sel_hi:[0,1,1]
	v_pk_fma_f32 v[10:11], s[40:41], v[96:97], v[10:11] op_sel_hi:[0,1,1]
	v_pk_fma_f32 v[12:13], s[40:41], v[98:99], v[12:13] op_sel_hi:[0,1,1]
	v_pk_fma_f32 v[6:7], s[48:49], v[96:97], v[6:7] op_sel_hi:[0,1,1]
	v_pk_fma_f32 v[8:9], s[48:49], v[98:99], v[8:9] op_sel_hi:[0,1,1]
	v_pk_fma_f32 v[2:3], s[56:57], v[96:97], v[2:3] op_sel_hi:[0,1,1]
	v_pk_fma_f32 v[4:5], s[56:57], v[98:99], v[4:5] op_sel_hi:[0,1,1]
	s_waitcnt vmcnt(14)
	v_pk_fma_f32 v[14:15], s[32:33], v[100:101], v[14:15] op_sel:[1,0,0]
	v_pk_fma_f32 v[16:17], s[32:33], v[102:103], v[16:17] op_sel:[1,0,0]
	v_pk_fma_f32 v[10:11], s[40:41], v[100:101], v[10:11] op_sel:[1,0,0]
	v_pk_fma_f32 v[12:13], s[40:41], v[102:103], v[12:13] op_sel:[1,0,0]
	v_pk_fma_f32 v[6:7], s[48:49], v[100:101], v[6:7] op_sel:[1,0,0]
	v_pk_fma_f32 v[8:9], s[48:49], v[102:103], v[8:9] op_sel:[1,0,0]
	v_pk_fma_f32 v[2:3], s[56:57], v[100:101], v[2:3] op_sel:[1,0,0]
	v_pk_fma_f32 v[4:5], s[56:57], v[102:103], v[4:5] op_sel:[1,0,0]
	s_waitcnt vmcnt(13)
	v_pk_fma_f32 v[14:15], s[34:35], v[104:105], v[14:15] op_sel_hi:[0,1,1]
	v_pk_fma_f32 v[16:17], s[34:35], v[106:107], v[16:17] op_sel_hi:[0,1,1]
	v_pk_fma_f32 v[10:11], s[42:43], v[104:105], v[10:11] op_sel_hi:[0,1,1]
	v_pk_fma_f32 v[12:13], s[42:43], v[106:107], v[12:13] op_sel_hi:[0,1,1]
	v_pk_fma_f32 v[6:7], s[50:51], v[104:105], v[6:7] op_sel_hi:[0,1,1]
	v_pk_fma_f32 v[8:9], s[50:51], v[106:107], v[8:9] op_sel_hi:[0,1,1]
	v_pk_fma_f32 v[2:3], s[58:59], v[104:105], v[2:3] op_sel_hi:[0,1,1]
	v_pk_fma_f32 v[4:5], s[58:59], v[106:107], v[4:5] op_sel_hi:[0,1,1]
	s_waitcnt vmcnt(12)
	v_pk_fma_f32 v[14:15], s[34:35], v[108:109], v[14:15] op_sel:[1,0,0]
	v_pk_fma_f32 v[16:17], s[34:35], v[110:111], v[16:17] op_sel:[1,0,0]
	v_pk_fma_f32 v[10:11], s[42:43], v[108:109], v[10:11] op_sel:[1,0,0]
	v_pk_fma_f32 v[12:13], s[42:43], v[110:111], v[12:13] op_sel:[1,0,0]
	v_pk_fma_f32 v[6:7], s[50:51], v[108:109], v[6:7] op_sel:[1,0,0]
	v_pk_fma_f32 v[8:9], s[50:51], v[110:111], v[8:9] op_sel:[1,0,0]
	v_pk_fma_f32 v[2:3], s[58:59], v[108:109], v[2:3] op_sel:[1,0,0]
	v_pk_fma_f32 v[4:5], s[58:59], v[110:111], v[4:5] op_sel:[1,0,0]
	s_waitcnt vmcnt(11)
	v_pk_fma_f32 v[14:15], s[36:37], v[112:113], v[14:15] op_sel_hi:[0,1,1]
	v_pk_fma_f32 v[16:17], s[36:37], v[114:115], v[16:17] op_sel_hi:[0,1,1]
	v_pk_fma_f32 v[10:11], s[44:45], v[112:113], v[10:11] op_sel_hi:[0,1,1]
	v_pk_fma_f32 v[12:13], s[44:45], v[114:115], v[12:13] op_sel_hi:[0,1,1]
	v_pk_fma_f32 v[6:7], s[52:53], v[112:113], v[6:7] op_sel_hi:[0,1,1]
	v_pk_fma_f32 v[8:9], s[52:53], v[114:115], v[8:9] op_sel_hi:[0,1,1]
	v_pk_fma_f32 v[2:3], s[60:61], v[112:113], v[2:3] op_sel_hi:[0,1,1]
	v_pk_fma_f32 v[4:5], s[60:61], v[114:115], v[4:5] op_sel_hi:[0,1,1]
	s_waitcnt vmcnt(10)
	v_pk_fma_f32 v[14:15], s[36:37], v[116:117], v[14:15] op_sel:[1,0,0]
	v_pk_fma_f32 v[16:17], s[36:37], v[118:119], v[16:17] op_sel:[1,0,0]
	v_pk_fma_f32 v[10:11], s[44:45], v[116:117], v[10:11] op_sel:[1,0,0]
	v_pk_fma_f32 v[12:13], s[44:45], v[118:119], v[12:13] op_sel:[1,0,0]
	v_pk_fma_f32 v[6:7], s[52:53], v[116:117], v[6:7] op_sel:[1,0,0]
	v_pk_fma_f32 v[8:9], s[52:53], v[118:119], v[8:9] op_sel:[1,0,0]
	v_pk_fma_f32 v[2:3], s[60:61], v[116:117], v[2:3] op_sel:[1,0,0]
	v_pk_fma_f32 v[4:5], s[60:61], v[118:119], v[4:5] op_sel:[1,0,0]
	s_waitcnt vmcnt(9)
	v_pk_fma_f32 v[14:15], s[38:39], v[120:121], v[14:15] op_sel_hi:[0,1,1]
	v_pk_fma_f32 v[16:17], s[38:39], v[122:123], v[16:17] op_sel_hi:[0,1,1]
	v_pk_fma_f32 v[10:11], s[46:47], v[120:121], v[10:11] op_sel_hi:[0,1,1]
	v_pk_fma_f32 v[12:13], s[46:47], v[122:123], v[12:13] op_sel_hi:[0,1,1]
	v_pk_fma_f32 v[6:7], s[54:55], v[120:121], v[6:7] op_sel_hi:[0,1,1]
	v_pk_fma_f32 v[8:9], s[54:55], v[122:123], v[8:9] op_sel_hi:[0,1,1]
	v_pk_fma_f32 v[2:3], s[62:63], v[120:121], v[2:3] op_sel_hi:[0,1,1]
	v_pk_fma_f32 v[4:5], s[62:63], v[122:123], v[4:5] op_sel_hi:[0,1,1]
	s_waitcnt vmcnt(8)
	v_pk_fma_f32 v[14:15], s[38:39], v[124:125], v[14:15] op_sel:[1,0,0]
	v_pk_fma_f32 v[16:17], s[38:39], v[126:127], v[16:17] op_sel:[1,0,0]
	v_pk_fma_f32 v[10:11], s[46:47], v[124:125], v[10:11] op_sel:[1,0,0]
	v_pk_fma_f32 v[12:13], s[46:47], v[126:127], v[12:13] op_sel:[1,0,0]
	v_pk_fma_f32 v[6:7], s[54:55], v[124:125], v[6:7] op_sel:[1,0,0]
	v_pk_fma_f32 v[8:9], s[54:55], v[126:127], v[8:9] op_sel:[1,0,0]
	v_pk_fma_f32 v[2:3], s[62:63], v[124:125], v[2:3] op_sel:[1,0,0]
	v_pk_fma_f32 v[4:5], s[62:63], v[126:127], v[4:5] op_sel:[1,0,0]
	s_waitcnt lgkmcnt(0)
	s_waitcnt vmcnt(7)
	v_pk_fma_f32 v[14:15], s[64:65], v[128:129], v[14:15] op_sel_hi:[0,1,1]
	v_pk_fma_f32 v[16:17], s[64:65], v[130:131], v[16:17] op_sel_hi:[0,1,1]
	v_pk_fma_f32 v[10:11], s[72:73], v[128:129], v[10:11] op_sel_hi:[0,1,1]
	v_pk_fma_f32 v[12:13], s[72:73], v[130:131], v[12:13] op_sel_hi:[0,1,1]
	v_pk_fma_f32 v[6:7], s[80:81], v[128:129], v[6:7] op_sel_hi:[0,1,1]
	v_pk_fma_f32 v[8:9], s[80:81], v[130:131], v[8:9] op_sel_hi:[0,1,1]
	v_pk_fma_f32 v[2:3], s[88:89], v[128:129], v[2:3] op_sel_hi:[0,1,1]
	v_pk_fma_f32 v[4:5], s[88:89], v[130:131], v[4:5] op_sel_hi:[0,1,1]
	s_waitcnt vmcnt(6)
	v_pk_fma_f32 v[14:15], s[64:65], v[132:133], v[14:15] op_sel:[1,0,0]
	v_pk_fma_f32 v[16:17], s[64:65], v[134:135], v[16:17] op_sel:[1,0,0]
	v_pk_fma_f32 v[10:11], s[72:73], v[132:133], v[10:11] op_sel:[1,0,0]
	v_pk_fma_f32 v[12:13], s[72:73], v[134:135], v[12:13] op_sel:[1,0,0]
	v_pk_fma_f32 v[6:7], s[80:81], v[132:133], v[6:7] op_sel:[1,0,0]
	v_pk_fma_f32 v[8:9], s[80:81], v[134:135], v[8:9] op_sel:[1,0,0]
	v_pk_fma_f32 v[2:3], s[88:89], v[132:133], v[2:3] op_sel:[1,0,0]
	v_pk_fma_f32 v[4:5], s[88:89], v[134:135], v[4:5] op_sel:[1,0,0]
	s_waitcnt vmcnt(5)
	v_pk_fma_f32 v[14:15], s[66:67], v[136:137], v[14:15] op_sel_hi:[0,1,1]
	v_pk_fma_f32 v[16:17], s[66:67], v[138:139], v[16:17] op_sel_hi:[0,1,1]
	v_pk_fma_f32 v[10:11], s[74:75], v[136:137], v[10:11] op_sel_hi:[0,1,1]
	v_pk_fma_f32 v[12:13], s[74:75], v[138:139], v[12:13] op_sel_hi:[0,1,1]
	v_pk_fma_f32 v[6:7], s[82:83], v[136:137], v[6:7] op_sel_hi:[0,1,1]
	v_pk_fma_f32 v[8:9], s[82:83], v[138:139], v[8:9] op_sel_hi:[0,1,1]
	v_pk_fma_f32 v[2:3], s[90:91], v[136:137], v[2:3] op_sel_hi:[0,1,1]
	v_pk_fma_f32 v[4:5], s[90:91], v[138:139], v[4:5] op_sel_hi:[0,1,1]
	s_waitcnt vmcnt(4)
	v_pk_fma_f32 v[14:15], s[66:67], v[140:141], v[14:15] op_sel:[1,0,0]
	v_pk_fma_f32 v[16:17], s[66:67], v[142:143], v[16:17] op_sel:[1,0,0]
	v_pk_fma_f32 v[10:11], s[74:75], v[140:141], v[10:11] op_sel:[1,0,0]
	v_pk_fma_f32 v[12:13], s[74:75], v[142:143], v[12:13] op_sel:[1,0,0]
	v_pk_fma_f32 v[6:7], s[82:83], v[140:141], v[6:7] op_sel:[1,0,0]
	v_pk_fma_f32 v[8:9], s[82:83], v[142:143], v[8:9] op_sel:[1,0,0]
	v_pk_fma_f32 v[2:3], s[90:91], v[140:141], v[2:3] op_sel:[1,0,0]
	v_pk_fma_f32 v[4:5], s[90:91], v[142:143], v[4:5] op_sel:[1,0,0]
	s_waitcnt vmcnt(3)
	v_pk_fma_f32 v[14:15], s[68:69], v[144:145], v[14:15] op_sel_hi:[0,1,1]
	v_pk_fma_f32 v[16:17], s[68:69], v[146:147], v[16:17] op_sel_hi:[0,1,1]
	v_pk_fma_f32 v[10:11], s[76:77], v[144:145], v[10:11] op_sel_hi:[0,1,1]
	v_pk_fma_f32 v[12:13], s[76:77], v[146:147], v[12:13] op_sel_hi:[0,1,1]
	v_pk_fma_f32 v[6:7], s[84:85], v[144:145], v[6:7] op_sel_hi:[0,1,1]
	v_pk_fma_f32 v[8:9], s[84:85], v[146:147], v[8:9] op_sel_hi:[0,1,1]
	v_pk_fma_f32 v[2:3], s[92:93], v[144:145], v[2:3] op_sel_hi:[0,1,1]
	v_pk_fma_f32 v[4:5], s[92:93], v[146:147], v[4:5] op_sel_hi:[0,1,1]
	s_waitcnt vmcnt(2)
	v_pk_fma_f32 v[14:15], s[68:69], v[148:149], v[14:15] op_sel:[1,0,0]
	v_pk_fma_f32 v[16:17], s[68:69], v[150:151], v[16:17] op_sel:[1,0,0]
	v_pk_fma_f32 v[10:11], s[76:77], v[148:149], v[10:11] op_sel:[1,0,0]
	v_pk_fma_f32 v[12:13], s[76:77], v[150:151], v[12:13] op_sel:[1,0,0]
	v_pk_fma_f32 v[6:7], s[84:85], v[148:149], v[6:7] op_sel:[1,0,0]
	v_pk_fma_f32 v[8:9], s[84:85], v[150:151], v[8:9] op_sel:[1,0,0]
	v_pk_fma_f32 v[2:3], s[92:93], v[148:149], v[2:3] op_sel:[1,0,0]
	v_pk_fma_f32 v[4:5], s[92:93], v[150:151], v[4:5] op_sel:[1,0,0]
	s_waitcnt vmcnt(1)
	v_pk_fma_f32 v[14:15], s[70:71], v[152:153], v[14:15] op_sel_hi:[0,1,1]
	v_pk_fma_f32 v[16:17], s[70:71], v[154:155], v[16:17] op_sel_hi:[0,1,1]
	v_pk_fma_f32 v[10:11], s[78:79], v[152:153], v[10:11] op_sel_hi:[0,1,1]
	v_pk_fma_f32 v[12:13], s[78:79], v[154:155], v[12:13] op_sel_hi:[0,1,1]
	v_pk_fma_f32 v[6:7], s[86:87], v[152:153], v[6:7] op_sel_hi:[0,1,1]
	v_pk_fma_f32 v[8:9], s[86:87], v[154:155], v[8:9] op_sel_hi:[0,1,1]
	v_pk_fma_f32 v[2:3], s[94:95], v[152:153], v[2:3] op_sel_hi:[0,1,1]
	v_pk_fma_f32 v[4:5], s[94:95], v[154:155], v[4:5] op_sel_hi:[0,1,1]
	s_waitcnt vmcnt(0)
	v_pk_fma_f32 v[14:15], s[70:71], v[156:157], v[14:15] op_sel:[1,0,0]
	v_pk_fma_f32 v[16:17], s[70:71], v[158:159], v[16:17] op_sel:[1,0,0]
	v_pk_fma_f32 v[10:11], s[78:79], v[156:157], v[10:11] op_sel:[1,0,0]
	v_pk_fma_f32 v[12:13], s[78:79], v[158:159], v[12:13] op_sel:[1,0,0]
	v_pk_fma_f32 v[6:7], s[86:87], v[156:157], v[6:7] op_sel:[1,0,0]
	v_pk_fma_f32 v[8:9], s[86:87], v[158:159], v[8:9] op_sel:[1,0,0]
	v_pk_fma_f32 v[2:3], s[94:95], v[156:157], v[2:3] op_sel:[1,0,0]
	v_pk_fma_f32 v[4:5], s[94:95], v[158:159], v[4:5] op_sel:[1,0,0]
	s_cmp_eq_u32 s22, 0
	s_cselect_b64 s[4:5], -1, 0
	s_and_b64 vcc, exec, s[4:5]
	s_cbranch_vccnz .LBB0_5
	v_lshl_or_b32 v1, s22, 13, v26
	v_add_u32_e32 v18, 0xffffe000, v1
	ds_write_b128 v18, v[14:17]
	v_add_u32_e32 v18, 0xffffe800, v1
	ds_write_b128 v18, v[10:13]
	v_add_u32_e32 v18, 0xfffff000, v1
	v_add_u32_e32 v1, 0xfffff800, v1
	ds_write_b128 v18, v[6:9]
	ds_write_b128 v1, v[2:5]

	.amdhsa_kernel _Z11prep_kernelPKfS0_S0_PDF16_PfPiS0_S1_
		.amdhsa_group_segment_fixed_size 24576
		.amdhsa_private_segment_fixed_size 0
		.amdhsa_kernarg_size 64
		.amdhsa_user_sgpr_count 2
		.amdhsa_user_sgpr_dispatch_ptr 0
		.amdhsa_user_sgpr_queue_ptr 0
		.amdhsa_user_sgpr_kernarg_segment_ptr 1
		.amdhsa_user_sgpr_dispatch_id 0
		.amdhsa_user_sgpr_kernarg_preload_length 0
		.amdhsa_user_sgpr_kernarg_preload_offset 0
		.amdhsa_user_sgpr_private_segment_size 0
		.amdhsa_uses_dynamic_stack 0
		.amdhsa_enable_private_segment 0
		.amdhsa_system_sgpr_workgroup_id_x 1
		.amdhsa_system_sgpr_workgroup_id_y 0
		.amdhsa_system_sgpr_workgroup_id_z 0
		.amdhsa_system_sgpr_workgroup_info 0
		.amdhsa_system_vgpr_workitem_id 0
		.amdhsa_next_free_vgpr 160
		.amdhsa_next_free_sgpr 96
		.amdhsa_accum_offset 160
		.amdhsa_reserve_vcc 1
		.amdhsa_float_round_mode_32 0
		.amdhsa_float_round_mode_16_64 0
		.amdhsa_float_denorm_mode_32 3
		.amdhsa_float_denorm_mode_16_64 3
		.amdhsa_dx10_clamp 1
		.amdhsa_ieee_mode 1
		.amdhsa_fp16_overflow 0
		.amdhsa_tg_split 0
		.amdhsa_exception_fp_ieee_invalid_op 0
		.amdhsa_exception_fp_denorm_src 0
		.amdhsa_exception_fp_ieee_div_zero 0
		.amdhsa_exception_fp_ieee_overflow 0
		.amdhsa_exception_fp_ieee_underflow 0
		.amdhsa_exception_fp_ieee_inexact 0
		.amdhsa_exception_int_div_zero 0
	.end_amdhsa_kernel

.LBB1_8:
	s_or_b64 exec, exec, s[8:9]
	v_mul_f32_e32 v131, 0x42c80000, v178
	s_mov_b32 s0, 0x24400
	s_mov_b32 s8, 0x3a000000
	s_lshl_b32 s11, s2, 9
	v_min3_f32 v130, v131, v130, 1.0
	v_or3_b32 v218, v162, v163, s0
	v_mov_b32_e32 v177, 0
	s_mov_b64 s[22:23], 0
	s_mov_b32 s0, 0
	s_mov_b32 s15, 0x45000000
	s_mov_b32 s9, 0x34800000
	s_mov_b32 s17, 0x3f7a4fa5
	s_mov_b32 s19, 0x403cf760
	s_mov_b32 s21, 0x40362960
	s_mov_b32 s10, 0x3dbaaaab
	s_mov_b32 s14, 0x3ee6024d
	s_mov_b32 s16, 0x3f26aaab
	s_mov_b32 s18, 0x3ea50e7e
	s_mov_b32 s20, 0x3e061862
	s_mov_b32 s28, 0x3aa1907f
	v_mov_b32_e32 v219, 0x358637bd
	v_mov_b32_e32 v220, 0x41200000
	s_mov_b32 s29, 0
	s_mov_b32 s30, 0
	v_mov_b32_e32 v221, 0
	s_waitcnt vmcnt(0) lgkmcnt(0)
	v_mov_b32_e32 v1, v130
	s_mov_b32 s40, 0x3a000000
	s_mov_b32 s41, 0x34800000
	s_mov_b32 s42, 0x45000000
	v_mul_f32_e32 v173, 0x44000000, v173
	v_mul_f32_e32 v172, 0x44000000, v172
	v_mul_f32_e32 v175, 0x44000000, v175
	v_mul_f32_e32 v174, 0x44000000, v174
	v_mov_b32_e32 v217, 0x24480
	v_mov_b64_e32 v[230:231], 0
	v_mov_b64_e32 v[232:233], 0
	v_mov_b64_e32 v[234:235], 0
	v_mov_b64_e32 v[236:237], 0
	ds_write_b128 v217, v[230:233]
	s_waitcnt lgkmcnt(0)
.Lrk_top:
	v_sub_f32_e32 v238, 1.0, v221
	v_min_f32_e32 v178, v1, v238
	v_cmp_eq_f32_e32 vcc, 0, v178
	v_mul_f32_e32 v178, 0x3b000000, v178
	s_cmp_eq_u64 vcc, exec
	s_cbranch_scc1 .Lrk_exit
	s_cmp_gt_i32 s30, 63
	s_cbranch_scc1 .Lrk_exit
	v_mul_f32_e32 v134, 0x3e4ccccd, v173
	v_mul_f32_e32 v142, 0x3e4ccccd, v172
	v_mul_f32_e32 v150, 0x3e4ccccd, v175
	v_mul_f32_e32 v158, 0x3e4ccccd, v174
	v_fma_mixlo_f16 v131, v178, v134, v171
	v_fma_mixlo_f16 v139, v178, v142, v170
	v_fma_mixlo_f16 v147, v178, v150, v169
	v_fma_mixlo_f16 v155, v178, v158, v168
	v_fma_f32 v130, v178, v134, v171
	v_fma_f32 v138, v178, v142, v170
	v_fma_f32 v146, v178, v150, v169
	v_fma_f32 v154, v178, v158, v168
	v_fma_mix_f32 v130, v130, 1.0, -v131 op_sel_hi:[0,0,1]
	v_fma_mix_f32 v138, v138, 1.0, -v139 op_sel_hi:[0,0,1]
	v_fma_mix_f32 v146, v146, 1.0, -v147 op_sel_hi:[0,0,1]
	v_fma_mix_f32 v154, v154, 1.0, -v155 op_sel_hi:[0,0,1]
	v_fma_mixlo_f16 v133, v130, s42, 0
	v_fma_mixlo_f16 v141, v138, s42, 0
	v_fma_mixlo_f16 v149, v146, s42, 0
	v_fma_mixlo_f16 v157, v154, s42, 0
	v_fma_mix_f32 v130, v130, s42, -v133 op_sel_hi:[0,0,1]
	v_fma_mix_f32 v138, v138, s42, -v141 op_sel_hi:[0,0,1]
	v_fma_mix_f32 v146, v146, s42, -v149 op_sel_hi:[0,0,1]
	v_fma_mix_f32 v154, v154, s42, -v157 op_sel_hi:[0,0,1]
	v_fma_mixlo_f16 v132, v130, s42, 0
	v_fma_mixlo_f16 v140, v138, s42, 0
	v_fma_mixlo_f16 v148, v146, s42, 0
	v_fma_mixlo_f16 v156, v154, s42, 0
	ds_write_b16 v204, v131
	ds_write_b16 v205, v139
	ds_write_b16 v206, v147
	ds_write_b16 v207, v155
	ds_write_b16 v204, v133 offset:544
	ds_write_b16 v205, v141 offset:544
	ds_write_b16 v206, v149 offset:544
	ds_write_b16 v207, v157 offset:544
	ds_write_b16 v204, v132 offset:1088
	ds_write_b16 v205, v140 offset:1088
	ds_write_b16 v206, v148 offset:1088
	ds_write_b16 v207, v156 offset:1088
	s_waitcnt lgkmcnt(0)
	s_barrier
	ds_read_b128 v[130:133], v208
	ds_read_b128 v[134:137], v209 offset:64
	ds_read_b128 v[138:141], v211
	ds_read_b128 v[142:145], v212
	ds_read_b128 v[146:149], v213
	ds_read_b128 v[150:153], v214
	ds_read_b128 v[154:157], v215
	ds_read_b128 v[158:161], v216
	ds_read_b128 v[180:183], v199 offset:0
	ds_read_b128 v[184:187], v199 offset:1024
	ds_read_b128 v[188:191], v199 offset:4096
	ds_read_b128 v[192:195], v199 offset:5120
	ds_read_b128 v[222:225], v199 offset:8192
	s_waitcnt lgkmcnt(6)
	ds_read_b128 v[226:229], v199 offset:9216
	v_smfmac_f32_16x16x64_f16 v[230:233], v[130:133], a[0:7], v210
	ds_read_b128 v[238:241], v217
	ds_read_b128 v[242:245], v217
	v_smfmac_f32_16x16x64_f16 v[234:237], v[130:133], v[18:25], v210
	v_mul_f32_e32 v166, 0x3d99999a, v173
	v_mul_f32_e32 v167, 0x3d99999a, v172
	v_smfmac_f32_16x16x64_f16 v[230:233], v[134:137], a[40:47], v210
	v_mul_f32_e32 v176, 0x3d99999a, v175
	v_mul_f32_e32 v177, 0x3d99999a, v174
	v_smfmac_f32_16x16x64_f16 v[234:237], v[134:137], v[34:41], v210
	v_smfmac_f32_16x16x64_f16 v[230:233], v[138:141], a[64:71], v210
	v_smfmac_f32_16x16x64_f16 v[234:237], v[138:141], v[42:49], v210
	v_smfmac_f32_16x16x64_f16 v[230:233], v[142:145], a[96:103], v210
	v_smfmac_f32_16x16x64_f16 v[234:237], v[142:145], v[58:65], v210
	v_smfmac_f32_16x16x64_f16 v[230:233], v[146:149], a[128:135], v210
	v_smfmac_f32_16x16x64_f16 v[234:237], v[146:149], v[74:81], v210
	v_smfmac_f32_16x16x64_f16 v[230:233], v[150:153], a[160:167], v210
	v_smfmac_f32_16x16x64_f16 v[234:237], v[150:153], v[98:105], v210
	v_smfmac_f32_16x16x64_f16 v[230:233], v[154:157], a[192:199], v210
	v_smfmac_f32_16x16x64_f16 v[234:237], v[154:157], v[106:113], v210
	s_waitcnt lgkmcnt(8)
	v_smfmac_f32_16x16x64_f16 v[230:233], v[158:161], a[224:231], v210
	v_smfmac_f32_16x16x64_f16 v[234:237], v[158:161], v[122:129], v210
	s_waitcnt lgkmcnt(1)
	v_smfmac_f32_16x16x64_f16 v[238:241], v[130:133], a[16:23], v210
	s_waitcnt lgkmcnt(0)
	v_smfmac_f32_16x16x64_f16 v[242:245], v[130:133], v[180:187], v210
	ds_read_b128 v[180:183], v199 offset:12288
	ds_read_b128 v[184:187], v199 offset:13312
	v_smfmac_f32_16x16x64_f16 v[238:241], v[134:137], a[48:55], v210
	v_fmac_f32_e32 v230, s40, v231
	v_fmac_f32_e32 v234, s40, v235
	v_smfmac_f32_16x16x64_f16 v[242:245], v[134:137], v[188:195], v210
	ds_read_b128 v[188:191], v199 offset:16384
	ds_read_b128 v[192:195], v199 offset:17408
	v_fmac_f32_e32 v230, s41, v232
	v_fmac_f32_e32 v234, s41, v236
	v_smfmac_f32_16x16x64_f16 v[238:241], v[138:141], a[80:87], v210
	s_nop 0
	v_permlane32_swap_b32_e32 v230, v234
	v_add_f32_e32 v162, v230, v234
	v_smfmac_f32_16x16x64_f16 v[242:245], v[138:141], v[222:229], v210
	ds_read_b128 v[222:225], v199 offset:20480
	ds_read_b128 v[226:229], v199 offset:21504
	v_fmac_f32_e32 v166, 0x3e666666, v162
	v_fma_mixlo_f16 v232, v178, v166, v171
	v_smfmac_f32_16x16x64_f16 v[238:241], v[142:145], a[112:119], v210
	v_fma_f32 v231, v178, v166, v171
	v_fma_mix_f32 v231, v231, 1.0, -v232 op_sel_hi:[0,0,1]
	s_waitcnt lgkmcnt(4)
	v_smfmac_f32_16x16x64_f16 v[242:245], v[142:145], v[180:187], v210
	ds_read_b128 v[180:183], v199 offset:24576
	ds_read_b128 v[184:187], v199 offset:25600
	v_fma_mixlo_f16 v235, v231, s42, 0
	v_fma_mix_f32 v231, v231, s42, -v235 op_sel_hi:[0,0,1]
	v_smfmac_f32_16x16x64_f16 v[238:241], v[146:149], a[144:151], v210
	v_fma_mixlo_f16 v233, v231, s42, 0
	ds_write_b16 v204, v232 offset:8704
	s_waitcnt lgkmcnt(5)
	v_smfmac_f32_16x16x64_f16 v[242:245], v[146:149], v[188:195], v210
	ds_read_b128 v[188:191], v199 offset:28672
	ds_read_b128 v[192:195], v199 offset:29696
	ds_write_b16 v204, v235 offset:9248
	ds_write_b16 v204, v233 offset:9792
	v_smfmac_f32_16x16x64_f16 v[238:241], v[150:153], a[176:183], v210
	ds_read_b128 v[230:233], v217
	ds_read_b128 v[234:237], v217
	s_waitcnt lgkmcnt(9)
	v_smfmac_f32_16x16x64_f16 v[242:245], v[150:153], v[222:229], v210
	ds_read_b128 v[222:225], v199 offset:2048
	ds_read_b128 v[226:229], v199 offset:3072
	v_smfmac_f32_16x16x64_f16 v[238:241], v[154:157], a[208:215], v210
	s_waitcnt lgkmcnt(9)
	v_smfmac_f32_16x16x64_f16 v[242:245], v[154:157], v[180:187], v210
	ds_read_b128 v[180:183], v199 offset:6144
	ds_read_b128 v[184:187], v199 offset:7168
	v_smfmac_f32_16x16x64_f16 v[238:241], v[158:161], a[240:247], v210
	s_waitcnt lgkmcnt(8)
	v_smfmac_f32_16x16x64_f16 v[242:245], v[158:161], v[188:195], v210
	ds_read_b128 v[188:191], v199 offset:10240
	ds_read_b128 v[192:195], v199 offset:11264
	s_waitcnt lgkmcnt(7)
	v_smfmac_f32_16x16x64_f16 v[230:233], v[130:133], a[8:15], v210
	s_waitcnt lgkmcnt(6)
	v_smfmac_f32_16x16x64_f16 v[234:237], v[130:133], v[2:9], v210
	v_smfmac_f32_16x16x64_f16 v[230:233], v[134:137], a[32:39], v210
	v_fmac_f32_e32 v238, s40, v239
	v_fmac_f32_e32 v242, s40, v243
	v_smfmac_f32_16x16x64_f16 v[234:237], v[134:137], v[10:17], v210
	v_fmac_f32_e32 v238, s41, v240
	v_fmac_f32_e32 v242, s41, v244
	v_smfmac_f32_16x16x64_f16 v[230:233], v[138:141], a[72:79], v210
	s_nop 0
	v_permlane32_swap_b32_e32 v238, v242
	v_add_f32_e32 v164, v238, v242
	v_smfmac_f32_16x16x64_f16 v[234:237], v[138:141], v[50:57], v210
	v_fmac_f32_e32 v176, 0x3e666666, v164
	v_fma_mixlo_f16 v240, v178, v176, v169
	v_smfmac_f32_16x16x64_f16 v[230:233], v[142:145], a[104:111], v210
	v_fma_f32 v239, v178, v176, v169
	v_fma_mix_f32 v239, v239, 1.0, -v240 op_sel_hi:[0,0,1]
	v_smfmac_f32_16x16x64_f16 v[234:237], v[142:145], v[26:33], v210
	v_fma_mixlo_f16 v243, v239, s42, 0
	v_fma_mix_f32 v239, v239, s42, -v243 op_sel_hi:[0,0,1]
	v_smfmac_f32_16x16x64_f16 v[230:233], v[146:149], a[136:143], v210
	v_fma_mixlo_f16 v241, v239, s42, 0
	ds_write_b16 v206, v240 offset:8704
	v_smfmac_f32_16x16x64_f16 v[234:237], v[146:149], v[82:89], v210
	ds_write_b16 v206, v243 offset:9248
	ds_write_b16 v206, v241 offset:9792
	v_smfmac_f32_16x16x64_f16 v[230:233], v[150:153], a[168:175], v210
	ds_read_b128 v[238:241], v217
	ds_read_b128 v[242:245], v217
	v_smfmac_f32_16x16x64_f16 v[234:237], v[150:153], v[66:73], v210
	v_smfmac_f32_16x16x64_f16 v[230:233], v[154:157], a[200:207], v210
	v_smfmac_f32_16x16x64_f16 v[234:237], v[154:157], v[114:121], v210
	v_smfmac_f32_16x16x64_f16 v[230:233], v[158:161], a[232:239], v210
	v_smfmac_f32_16x16x64_f16 v[234:237], v[158:161], v[90:97], v210
	s_waitcnt lgkmcnt(1)
	v_smfmac_f32_16x16x64_f16 v[238:241], v[130:133], a[24:31], v210
	s_waitcnt lgkmcnt(0)
	v_smfmac_f32_16x16x64_f16 v[242:245], v[130:133], v[222:229], v210
	ds_read_b128 v[222:225], v199 offset:14336
	ds_read_b128 v[226:229], v199 offset:15360
	v_smfmac_f32_16x16x64_f16 v[238:241], v[134:137], a[56:63], v210
	v_fmac_f32_e32 v230, s40, v231
	v_fmac_f32_e32 v234, s40, v235
	v_smfmac_f32_16x16x64_f16 v[242:245], v[134:137], v[180:187], v210
	ds_read_b128 v[180:183], v199 offset:18432
	ds_read_b128 v[184:187], v199 offset:19456
	v_fmac_f32_e32 v230, s41, v232
	v_fmac_f32_e32 v234, s41, v236
	v_smfmac_f32_16x16x64_f16 v[238:241], v[138:141], a[88:95], v210
	s_nop 0
	v_permlane32_swap_b32_e32 v230, v234
	v_add_f32_e32 v163, v230, v234
	v_smfmac_f32_16x16x64_f16 v[242:245], v[138:141], v[188:195], v210
	ds_read_b128 v[188:191], v199 offset:22528
	ds_read_b128 v[192:195], v199 offset:23552
	v_fmac_f32_e32 v167, 0x3e666666, v163
	v_fma_mixlo_f16 v232, v178, v167, v170
	v_smfmac_f32_16x16x64_f16 v[238:241], v[142:145], a[120:127], v210
	v_fma_f32 v231, v178, v167, v170
	v_fma_mix_f32 v231, v231, 1.0, -v232 op_sel_hi:[0,0,1]
	s_waitcnt lgkmcnt(4)
	v_smfmac_f32_16x16x64_f16 v[242:245], v[142:145], v[222:229], v210
	ds_read_b128 v[222:225], v199 offset:26624
	ds_read_b128 v[226:229], v199 offset:27648
	v_fma_mixlo_f16 v235, v231, s42, 0
	v_fma_mix_f32 v231, v231, s42, -v235 op_sel_hi:[0,0,1]
	v_smfmac_f32_16x16x64_f16 v[238:241], v[146:149], a[152:159], v210
	v_fma_mixlo_f16 v233, v231, s42, 0
	ds_write_b16 v205, v232 offset:8704
	s_waitcnt lgkmcnt(5)
	v_smfmac_f32_16x16x64_f16 v[242:245], v[146:149], v[180:187], v210
	ds_read_b128 v[180:183], v199 offset:30720
	ds_read_b128 v[184:187], v199 offset:31744
	ds_write_b16 v205, v235 offset:9248
	ds_write_b16 v205, v233 offset:9792
	v_smfmac_f32_16x16x64_f16 v[238:241], v[150:153], a[184:191], v210
	ds_read_b128 v[230:233], v217
	ds_read_b128 v[234:237], v217
	s_waitcnt lgkmcnt(9)
	v_smfmac_f32_16x16x64_f16 v[242:245], v[150:153], v[188:195], v210
	v_smfmac_f32_16x16x64_f16 v[238:241], v[154:157], a[216:223], v210
	s_waitcnt lgkmcnt(7)
	v_smfmac_f32_16x16x64_f16 v[242:245], v[154:157], v[222:229], v210
	v_smfmac_f32_16x16x64_f16 v[238:241], v[158:161], a[248:255], v210
	s_waitcnt lgkmcnt(4)
	v_smfmac_f32_16x16x64_f16 v[242:245], v[158:161], v[180:187], v210
	s_nop 5
	v_fmac_f32_e32 v238, s40, v239
	s_nop 0
	v_fmac_f32_e32 v242, s40, v243
	v_fmac_f32_e32 v238, s41, v240
	v_fmac_f32_e32 v242, s41, v244
	s_nop 1
	v_permlane32_swap_b32_e32 v238, v242
	v_add_f32_e32 v165, v238, v242
	v_fmac_f32_e32 v177, 0x3e666666, v165
	v_fma_mixlo_f16 v240, v178, v177, v168
	v_fma_f32 v239, v178, v177, v168
	v_fma_mix_f32 v239, v239, 1.0, -v240 op_sel_hi:[0,0,1]
	v_fma_mixlo_f16 v243, v239, s42, 0
	v_fma_mix_f32 v239, v239, s42, -v243 op_sel_hi:[0,0,1]
	v_fma_mixlo_f16 v241, v239, s42, 0
	ds_write_b16 v207, v240 offset:8704
	ds_write_b16 v207, v243 offset:9248
	ds_write_b16 v207, v241 offset:9792
	s_waitcnt lgkmcnt(0)
	s_barrier
	ds_read_b128 v[130:133], v208 offset:8704
	ds_read_b128 v[134:137], v209 offset:8768
	ds_read_b128 v[138:141], v211 offset:8704
	ds_read_b128 v[142:145], v212 offset:8704
	ds_read_b128 v[146:149], v213 offset:8704
	ds_read_b128 v[150:153], v214 offset:8704
	ds_read_b128 v[154:157], v215 offset:8704
	ds_read_b128 v[158:161], v216 offset:8704
	ds_read_b128 v[180:183], v199 offset:0
	ds_read_b128 v[184:187], v199 offset:1024
	ds_read_b128 v[188:191], v199 offset:4096
	ds_read_b128 v[192:195], v199 offset:5120
	ds_read_b128 v[222:225], v199 offset:8192
	s_waitcnt lgkmcnt(6)
	ds_read_b128 v[226:229], v199 offset:9216
	v_smfmac_f32_16x16x64_f16 v[230:233], v[130:133], a[0:7], v210
	ds_read_b128 v[238:241], v217
	ds_read_b128 v[242:245], v217
	v_smfmac_f32_16x16x64_f16 v[234:237], v[130:133], v[18:25], v210
	v_mul_f32_e32 v179, 0x3f7a4fa5, v173
	v_fmac_f32_e32 v179, 0xc06eeeef, v162
	v_smfmac_f32_16x16x64_f16 v[230:233], v[134:137], a[40:47], v210
	v_mul_f32_e32 v196, 0x3f7a4fa5, v172
	v_fmac_f32_e32 v196, 0xc06eeeef, v163
	v_smfmac_f32_16x16x64_f16 v[234:237], v[134:137], v[34:41], v210
	v_mul_f32_e32 v197, 0x3f7a4fa5, v175
	v_fmac_f32_e32 v197, 0xc06eeeef, v164
	v_smfmac_f32_16x16x64_f16 v[230:233], v[138:141], a[64:71], v210
	v_mul_f32_e32 v198, 0x3f7a4fa5, v174
	v_fmac_f32_e32 v198, 0xc06eeeef, v165
	v_smfmac_f32_16x16x64_f16 v[234:237], v[138:141], v[42:49], v210
	v_smfmac_f32_16x16x64_f16 v[230:233], v[142:145], a[96:103], v210
	v_smfmac_f32_16x16x64_f16 v[234:237], v[142:145], v[58:65], v210
	v_smfmac_f32_16x16x64_f16 v[230:233], v[146:149], a[128:135], v210
	v_smfmac_f32_16x16x64_f16 v[234:237], v[146:149], v[74:81], v210
	v_smfmac_f32_16x16x64_f16 v[230:233], v[150:153], a[160:167], v210
	v_smfmac_f32_16x16x64_f16 v[234:237], v[150:153], v[98:105], v210
	v_smfmac_f32_16x16x64_f16 v[230:233], v[154:157], a[192:199], v210
	v_smfmac_f32_16x16x64_f16 v[234:237], v[154:157], v[106:113], v210
	s_waitcnt lgkmcnt(8)
	v_smfmac_f32_16x16x64_f16 v[230:233], v[158:161], a[224:231], v210
	v_smfmac_f32_16x16x64_f16 v[234:237], v[158:161], v[122:129], v210
	s_waitcnt lgkmcnt(1)
	v_smfmac_f32_16x16x64_f16 v[238:241], v[130:133], a[16:23], v210
	s_waitcnt lgkmcnt(0)
	v_smfmac_f32_16x16x64_f16 v[242:245], v[130:133], v[180:187], v210
	ds_read_b128 v[180:183], v199 offset:12288
	ds_read_b128 v[184:187], v199 offset:13312
	v_smfmac_f32_16x16x64_f16 v[238:241], v[134:137], a[48:55], v210
	v_fmac_f32_e32 v230, s40, v231
	v_fmac_f32_e32 v234, s40, v235
	v_smfmac_f32_16x16x64_f16 v[242:245], v[134:137], v[188:195], v210
	ds_read_b128 v[188:191], v199 offset:16384
	ds_read_b128 v[192:195], v199 offset:17408
	v_fmac_f32_e32 v230, s41, v232
	v_fmac_f32_e32 v234, s41, v236
	v_smfmac_f32_16x16x64_f16 v[238:241], v[138:141], a[80:87], v210
	s_nop 0
	v_permlane32_swap_b32_e32 v230, v234
	v_add_f32_e32 v166, v230, v234
	v_smfmac_f32_16x16x64_f16 v[242:245], v[138:141], v[222:229], v210
	ds_read_b128 v[222:225], v199 offset:20480
	ds_read_b128 v[226:229], v199 offset:21504
	v_fmac_f32_e32 v179, 0x40638e39, v166
	v_fma_mixlo_f16 v232, v178, v179, v171
	v_smfmac_f32_16x16x64_f16 v[238:241], v[142:145], a[112:119], v210
	v_fma_f32 v231, v178, v179, v171
	v_fma_mix_f32 v231, v231, 1.0, -v232 op_sel_hi:[0,0,1]
	s_waitcnt lgkmcnt(4)
	v_smfmac_f32_16x16x64_f16 v[242:245], v[142:145], v[180:187], v210
	ds_read_b128 v[180:183], v199 offset:24576
	ds_read_b128 v[184:187], v199 offset:25600
	v_fma_mixlo_f16 v235, v231, s42, 0
	v_fma_mix_f32 v231, v231, s42, -v235 op_sel_hi:[0,0,1]
	v_smfmac_f32_16x16x64_f16 v[238:241], v[146:149], a[144:151], v210
	v_fma_mixlo_f16 v233, v231, s42, 0
	ds_write_b16 v204, v232
	s_waitcnt lgkmcnt(5)
	v_smfmac_f32_16x16x64_f16 v[242:245], v[146:149], v[188:195], v210
	ds_read_b128 v[188:191], v199 offset:28672
	ds_read_b128 v[192:195], v199 offset:29696
	ds_write_b16 v204, v235 offset:544
	ds_write_b16 v204, v233 offset:1088
	v_smfmac_f32_16x16x64_f16 v[238:241], v[150:153], a[176:183], v210
	ds_read_b128 v[230:233], v217
	ds_read_b128 v[234:237], v217
	s_waitcnt lgkmcnt(9)
	v_smfmac_f32_16x16x64_f16 v[242:245], v[150:153], v[222:229], v210
	ds_read_b128 v[222:225], v199 offset:2048
	ds_read_b128 v[226:229], v199 offset:3072
	v_smfmac_f32_16x16x64_f16 v[238:241], v[154:157], a[208:215], v210
	s_waitcnt lgkmcnt(9)
	v_smfmac_f32_16x16x64_f16 v[242:245], v[154:157], v[180:187], v210
	ds_read_b128 v[180:183], v199 offset:6144
	ds_read_b128 v[184:187], v199 offset:7168
	v_smfmac_f32_16x16x64_f16 v[238:241], v[158:161], a[240:247], v210
	s_waitcnt lgkmcnt(8)
	v_smfmac_f32_16x16x64_f16 v[242:245], v[158:161], v[188:195], v210
	ds_read_b128 v[188:191], v199 offset:10240
	ds_read_b128 v[192:195], v199 offset:11264
	s_waitcnt lgkmcnt(7)
	v_smfmac_f32_16x16x64_f16 v[230:233], v[130:133], a[8:15], v210
	s_waitcnt lgkmcnt(6)
	v_smfmac_f32_16x16x64_f16 v[234:237], v[130:133], v[2:9], v210
	v_smfmac_f32_16x16x64_f16 v[230:233], v[134:137], a[32:39], v210
	v_fmac_f32_e32 v238, s40, v239
	v_fmac_f32_e32 v242, s40, v243
	v_smfmac_f32_16x16x64_f16 v[234:237], v[134:137], v[10:17], v210
	v_fmac_f32_e32 v238, s41, v240
	v_fmac_f32_e32 v242, s41, v244
	v_smfmac_f32_16x16x64_f16 v[230:233], v[138:141], a[72:79], v210
	s_nop 0
	v_permlane32_swap_b32_e32 v238, v242
	v_add_f32_e32 v176, v238, v242
	v_smfmac_f32_16x16x64_f16 v[234:237], v[138:141], v[50:57], v210
	v_fmac_f32_e32 v197, 0x40638e39, v176
	v_fma_mixlo_f16 v240, v178, v197, v169
	v_smfmac_f32_16x16x64_f16 v[230:233], v[142:145], a[104:111], v210
	v_fma_f32 v239, v178, v197, v169
	v_fma_mix_f32 v239, v239, 1.0, -v240 op_sel_hi:[0,0,1]
	v_smfmac_f32_16x16x64_f16 v[234:237], v[142:145], v[26:33], v210
	v_fma_mixlo_f16 v243, v239, s42, 0
	v_fma_mix_f32 v239, v239, s42, -v243 op_sel_hi:[0,0,1]
	v_smfmac_f32_16x16x64_f16 v[230:233], v[146:149], a[136:143], v210
	v_fma_mixlo_f16 v241, v239, s42, 0
	ds_write_b16 v206, v240
	v_smfmac_f32_16x16x64_f16 v[234:237], v[146:149], v[82:89], v210
	ds_write_b16 v206, v243 offset:544
	ds_write_b16 v206, v241 offset:1088
	v_smfmac_f32_16x16x64_f16 v[230:233], v[150:153], a[168:175], v210
	ds_read_b128 v[238:241], v217
	ds_read_b128 v[242:245], v217
	v_smfmac_f32_16x16x64_f16 v[234:237], v[150:153], v[66:73], v210
	v_smfmac_f32_16x16x64_f16 v[230:233], v[154:157], a[200:207], v210
	v_smfmac_f32_16x16x64_f16 v[234:237], v[154:157], v[114:121], v210
	v_smfmac_f32_16x16x64_f16 v[230:233], v[158:161], a[232:239], v210
	v_smfmac_f32_16x16x64_f16 v[234:237], v[158:161], v[90:97], v210
	s_waitcnt lgkmcnt(1)
	v_smfmac_f32_16x16x64_f16 v[238:241], v[130:133], a[24:31], v210
	s_waitcnt lgkmcnt(0)
	v_smfmac_f32_16x16x64_f16 v[242:245], v[130:133], v[222:229], v210
	ds_read_b128 v[222:225], v199 offset:14336
	ds_read_b128 v[226:229], v199 offset:15360
	v_smfmac_f32_16x16x64_f16 v[238:241], v[134:137], a[56:63], v210
	v_fmac_f32_e32 v230, s40, v231
	v_fmac_f32_e32 v234, s40, v235
	v_smfmac_f32_16x16x64_f16 v[242:245], v[134:137], v[180:187], v210
	ds_read_b128 v[180:183], v199 offset:18432
	ds_read_b128 v[184:187], v199 offset:19456
	v_fmac_f32_e32 v230, s41, v232
	v_fmac_f32_e32 v234, s41, v236
	v_smfmac_f32_16x16x64_f16 v[238:241], v[138:141], a[88:95], v210
	s_nop 0
	v_permlane32_swap_b32_e32 v230, v234
	v_add_f32_e32 v167, v230, v234
	v_smfmac_f32_16x16x64_f16 v[242:245], v[138:141], v[188:195], v210
	ds_read_b128 v[188:191], v199 offset:22528
	ds_read_b128 v[192:195], v199 offset:23552
	v_fmac_f32_e32 v196, 0x40638e39, v167
	v_fma_mixlo_f16 v232, v178, v196, v170
	v_smfmac_f32_16x16x64_f16 v[238:241], v[142:145], a[120:127], v210
	v_fma_f32 v231, v178, v196, v170
	v_fma_mix_f32 v231, v231, 1.0, -v232 op_sel_hi:[0,0,1]
	s_waitcnt lgkmcnt(4)
	v_smfmac_f32_16x16x64_f16 v[242:245], v[142:145], v[222:229], v210
	ds_read_b128 v[222:225], v199 offset:26624
	ds_read_b128 v[226:229], v199 offset:27648
	v_fma_mixlo_f16 v235, v231, s42, 0
	v_fma_mix_f32 v231, v231, s42, -v235 op_sel_hi:[0,0,1]
	v_smfmac_f32_16x16x64_f16 v[238:241], v[146:149], a[152:159], v210
	v_fma_mixlo_f16 v233, v231, s42, 0
	ds_write_b16 v205, v232
	s_waitcnt lgkmcnt(5)
	v_smfmac_f32_16x16x64_f16 v[242:245], v[146:149], v[180:187], v210
	ds_read_b128 v[180:183], v199 offset:30720
	ds_read_b128 v[184:187], v199 offset:31744
	ds_write_b16 v205, v235 offset:544
	ds_write_b16 v205, v233 offset:1088
	v_smfmac_f32_16x16x64_f16 v[238:241], v[150:153], a[184:191], v210
	ds_read_b128 v[230:233], v217
	ds_read_b128 v[234:237], v217
	s_waitcnt lgkmcnt(9)
	v_smfmac_f32_16x16x64_f16 v[242:245], v[150:153], v[188:195], v210
	v_smfmac_f32_16x16x64_f16 v[238:241], v[154:157], a[216:223], v210
	s_waitcnt lgkmcnt(7)
	v_smfmac_f32_16x16x64_f16 v[242:245], v[154:157], v[222:229], v210
	v_smfmac_f32_16x16x64_f16 v[238:241], v[158:161], a[248:255], v210
	s_waitcnt lgkmcnt(4)
	v_smfmac_f32_16x16x64_f16 v[242:245], v[158:161], v[180:187], v210
	s_nop 5
	v_fmac_f32_e32 v238, s40, v239
	s_nop 0
	v_fmac_f32_e32 v242, s40, v243
	v_fmac_f32_e32 v238, s41, v240
	v_fmac_f32_e32 v242, s41, v244
	s_nop 1
	v_permlane32_swap_b32_e32 v238, v242
	v_add_f32_e32 v177, v238, v242
	v_fmac_f32_e32 v198, 0x40638e39, v177
	v_fma_mixlo_f16 v240, v178, v198, v168
	v_fma_f32 v239, v178, v198, v168
	v_fma_mix_f32 v239, v239, 1.0, -v240 op_sel_hi:[0,0,1]
	v_fma_mixlo_f16 v243, v239, s42, 0
	v_fma_mix_f32 v239, v239, s42, -v243 op_sel_hi:[0,0,1]
	v_fma_mixlo_f16 v241, v239, s42, 0
	ds_write_b16 v207, v240
	ds_write_b16 v207, v243 offset:544
	ds_write_b16 v207, v241 offset:1088
	s_waitcnt lgkmcnt(0)
	s_barrier
	ds_read_b128 v[130:133], v208
	ds_read_b128 v[134:137], v209 offset:64
	ds_read_b128 v[138:141], v211
	ds_read_b128 v[142:145], v212
	ds_read_b128 v[146:149], v213
	ds_read_b128 v[150:153], v214
	ds_read_b128 v[154:157], v215
	ds_read_b128 v[158:161], v216
	ds_read_b128 v[180:183], v199 offset:0
	ds_read_b128 v[184:187], v199 offset:1024
	ds_read_b128 v[188:191], v199 offset:4096
	ds_read_b128 v[192:195], v199 offset:5120
	ds_read_b128 v[222:225], v199 offset:8192
	s_waitcnt lgkmcnt(6)
	ds_read_b128 v[226:229], v199 offset:9216
	v_smfmac_f32_16x16x64_f16 v[230:233], v[130:133], a[0:7], v210
	ds_read_b128 v[238:241], v217
	ds_read_b128 v[242:245], v217
	v_smfmac_f32_16x16x64_f16 v[234:237], v[130:133], v[18:25], v210
	v_mul_f32_e32 v219, 0x403cf760, v173
	v_fmac_f32_e32 v219, 0xc139885f, v162
	v_smfmac_f32_16x16x64_f16 v[230:233], v[134:137], a[40:47], v210
	v_fmac_f32_e32 v219, 0x411d2a92, v166
	v_mul_f32_e32 v220, 0x403cf760, v172
	v_smfmac_f32_16x16x64_f16 v[234:237], v[134:137], v[34:41], v210
	v_fmac_f32_e32 v220, 0xc139885f, v163
	v_fmac_f32_e32 v220, 0x411d2a92, v167
	v_smfmac_f32_16x16x64_f16 v[230:233], v[138:141], a[64:71], v210
	v_mul_f32_e32 v246, 0x403cf760, v175
	v_fmac_f32_e32 v246, 0xc139885f, v164
	v_smfmac_f32_16x16x64_f16 v[234:237], v[138:141], v[42:49], v210
	v_fmac_f32_e32 v246, 0x411d2a92, v176
	v_mul_f32_e32 v247, 0x403cf760, v174
	v_smfmac_f32_16x16x64_f16 v[230:233], v[142:145], a[96:103], v210
	v_fmac_f32_e32 v247, 0xc139885f, v165
	v_fmac_f32_e32 v247, 0x411d2a92, v177
	v_smfmac_f32_16x16x64_f16 v[234:237], v[142:145], v[58:65], v210
	v_smfmac_f32_16x16x64_f16 v[230:233], v[146:149], a[128:135], v210
	v_smfmac_f32_16x16x64_f16 v[234:237], v[146:149], v[74:81], v210
	v_smfmac_f32_16x16x64_f16 v[230:233], v[150:153], a[160:167], v210
	v_smfmac_f32_16x16x64_f16 v[234:237], v[150:153], v[98:105], v210
	v_smfmac_f32_16x16x64_f16 v[230:233], v[154:157], a[192:199], v210
	v_smfmac_f32_16x16x64_f16 v[234:237], v[154:157], v[106:113], v210
	s_waitcnt lgkmcnt(8)
	v_smfmac_f32_16x16x64_f16 v[230:233], v[158:161], a[224:231], v210
	v_smfmac_f32_16x16x64_f16 v[234:237], v[158:161], v[122:129], v210
	s_waitcnt lgkmcnt(1)
	v_smfmac_f32_16x16x64_f16 v[238:241], v[130:133], a[16:23], v210
	s_waitcnt lgkmcnt(0)
	v_smfmac_f32_16x16x64_f16 v[242:245], v[130:133], v[180:187], v210
	ds_read_b128 v[180:183], v199 offset:12288
	ds_read_b128 v[184:187], v199 offset:13312
	v_smfmac_f32_16x16x64_f16 v[238:241], v[134:137], a[48:55], v210
	v_fmac_f32_e32 v230, s40, v231
	v_fmac_f32_e32 v234, s40, v235
	v_smfmac_f32_16x16x64_f16 v[242:245], v[134:137], v[188:195], v210
	ds_read_b128 v[188:191], v199 offset:16384
	ds_read_b128 v[192:195], v199 offset:17408
	v_fmac_f32_e32 v230, s41, v232
	v_fmac_f32_e32 v234, s41, v236
	v_smfmac_f32_16x16x64_f16 v[238:241], v[138:141], a[80:87], v210
	s_nop 0
	v_permlane32_swap_b32_e32 v230, v234
	v_add_f32_e32 v179, v230, v234
	v_smfmac_f32_16x16x64_f16 v[242:245], v[138:141], v[222:229], v210
	ds_read_b128 v[222:225], v199 offset:20480
	ds_read_b128 v[226:229], v199 offset:21504
	v_fmac_f32_e32 v219, 0xbe94e4f6, v179
	v_fma_mixlo_f16 v232, v178, v219, v171
	v_smfmac_f32_16x16x64_f16 v[238:241], v[142:145], a[112:119], v210
	v_fma_f32 v231, v178, v219, v171
	v_fma_mix_f32 v231, v231, 1.0, -v232 op_sel_hi:[0,0,1]
	s_waitcnt lgkmcnt(4)
	v_smfmac_f32_16x16x64_f16 v[242:245], v[142:145], v[180:187], v210
	ds_read_b128 v[180:183], v199 offset:24576
	ds_read_b128 v[184:187], v199 offset:25600
	v_fma_mixlo_f16 v235, v231, s42, 0
	v_fma_mix_f32 v231, v231, s42, -v235 op_sel_hi:[0,0,1]
	v_smfmac_f32_16x16x64_f16 v[238:241], v[146:149], a[144:151], v210
	v_fma_mixlo_f16 v233, v231, s42, 0
	ds_write_b16 v204, v232 offset:8704
	s_waitcnt lgkmcnt(5)
	v_smfmac_f32_16x16x64_f16 v[242:245], v[146:149], v[188:195], v210
	ds_read_b128 v[188:191], v199 offset:28672
	ds_read_b128 v[192:195], v199 offset:29696
	ds_write_b16 v204, v235 offset:9248
	ds_write_b16 v204, v233 offset:9792
	v_smfmac_f32_16x16x64_f16 v[238:241], v[150:153], a[176:183], v210
	ds_read_b128 v[230:233], v217
	ds_read_b128 v[234:237], v217
	s_waitcnt lgkmcnt(9)
	v_smfmac_f32_16x16x64_f16 v[242:245], v[150:153], v[222:229], v210
	ds_read_b128 v[222:225], v199 offset:2048
	ds_read_b128 v[226:229], v199 offset:3072
	v_smfmac_f32_16x16x64_f16 v[238:241], v[154:157], a[208:215], v210
	s_waitcnt lgkmcnt(9)
	v_smfmac_f32_16x16x64_f16 v[242:245], v[154:157], v[180:187], v210
	ds_read_b128 v[180:183], v199 offset:6144
	ds_read_b128 v[184:187], v199 offset:7168
	v_smfmac_f32_16x16x64_f16 v[238:241], v[158:161], a[240:247], v210
	s_waitcnt lgkmcnt(8)
	v_smfmac_f32_16x16x64_f16 v[242:245], v[158:161], v[188:195], v210
	ds_read_b128 v[188:191], v199 offset:10240
	ds_read_b128 v[192:195], v199 offset:11264
	s_waitcnt lgkmcnt(7)
	v_smfmac_f32_16x16x64_f16 v[230:233], v[130:133], a[8:15], v210
	s_waitcnt lgkmcnt(6)
	v_smfmac_f32_16x16x64_f16 v[234:237], v[130:133], v[2:9], v210
	v_smfmac_f32_16x16x64_f16 v[230:233], v[134:137], a[32:39], v210
	v_fmac_f32_e32 v238, s40, v239
	v_fmac_f32_e32 v242, s40, v243
	v_smfmac_f32_16x16x64_f16 v[234:237], v[134:137], v[10:17], v210
	v_fmac_f32_e32 v238, s41, v240
	v_fmac_f32_e32 v242, s41, v244
	v_smfmac_f32_16x16x64_f16 v[230:233], v[138:141], a[72:79], v210
	s_nop 0
	v_permlane32_swap_b32_e32 v238, v242
	v_add_f32_e32 v197, v238, v242
	v_smfmac_f32_16x16x64_f16 v[234:237], v[138:141], v[50:57], v210
	v_fmac_f32_e32 v246, 0xbe94e4f6, v197
	v_fma_mixlo_f16 v240, v178, v246, v169
	v_smfmac_f32_16x16x64_f16 v[230:233], v[142:145], a[104:111], v210
	v_fma_f32 v239, v178, v246, v169
	v_fma_mix_f32 v239, v239, 1.0, -v240 op_sel_hi:[0,0,1]
	v_smfmac_f32_16x16x64_f16 v[234:237], v[142:145], v[26:33], v210
	v_fma_mixlo_f16 v243, v239, s42, 0
	v_fma_mix_f32 v239, v239, s42, -v243 op_sel_hi:[0,0,1]
	v_smfmac_f32_16x16x64_f16 v[230:233], v[146:149], a[136:143], v210
	v_fma_mixlo_f16 v241, v239, s42, 0
	ds_write_b16 v206, v240 offset:8704
	v_smfmac_f32_16x16x64_f16 v[234:237], v[146:149], v[82:89], v210
	ds_write_b16 v206, v243 offset:9248
	ds_write_b16 v206, v241 offset:9792
	v_smfmac_f32_16x16x64_f16 v[230:233], v[150:153], a[168:175], v210
	ds_read_b128 v[238:241], v217
	ds_read_b128 v[242:245], v217
	v_smfmac_f32_16x16x64_f16 v[234:237], v[150:153], v[66:73], v210
	v_smfmac_f32_16x16x64_f16 v[230:233], v[154:157], a[200:207], v210
	v_smfmac_f32_16x16x64_f16 v[234:237], v[154:157], v[114:121], v210
	v_smfmac_f32_16x16x64_f16 v[230:233], v[158:161], a[232:239], v210
	v_smfmac_f32_16x16x64_f16 v[234:237], v[158:161], v[90:97], v210
	s_waitcnt lgkmcnt(1)
	v_smfmac_f32_16x16x64_f16 v[238:241], v[130:133], a[24:31], v210
	s_waitcnt lgkmcnt(0)
	v_smfmac_f32_16x16x64_f16 v[242:245], v[130:133], v[222:229], v210
	ds_read_b128 v[222:225], v199 offset:14336
	ds_read_b128 v[226:229], v199 offset:15360
	v_smfmac_f32_16x16x64_f16 v[238:241], v[134:137], a[56:63], v210
	v_fmac_f32_e32 v230, s40, v231
	v_fmac_f32_e32 v234, s40, v235
	v_smfmac_f32_16x16x64_f16 v[242:245], v[134:137], v[180:187], v210
	ds_read_b128 v[180:183], v199 offset:18432
	ds_read_b128 v[184:187], v199 offset:19456
	v_fmac_f32_e32 v230, s41, v232
	v_fmac_f32_e32 v234, s41, v236
	v_smfmac_f32_16x16x64_f16 v[238:241], v[138:141], a[88:95], v210
	s_nop 0
	v_permlane32_swap_b32_e32 v230, v234
	v_add_f32_e32 v196, v230, v234
	v_smfmac_f32_16x16x64_f16 v[242:245], v[138:141], v[188:195], v210
	ds_read_b128 v[188:191], v199 offset:22528
	ds_read_b128 v[192:195], v199 offset:23552
	v_fmac_f32_e32 v220, 0xbe94e4f6, v196
	v_fma_mixlo_f16 v232, v178, v220, v170
	v_smfmac_f32_16x16x64_f16 v[238:241], v[142:145], a[120:127], v210
	v_fma_f32 v231, v178, v220, v170
	v_fma_mix_f32 v231, v231, 1.0, -v232 op_sel_hi:[0,0,1]
	s_waitcnt lgkmcnt(4)
	v_smfmac_f32_16x16x64_f16 v[242:245], v[142:145], v[222:229], v210
	ds_read_b128 v[222:225], v199 offset:26624
	ds_read_b128 v[226:229], v199 offset:27648
	v_fma_mixlo_f16 v235, v231, s42, 0
	v_fma_mix_f32 v231, v231, s42, -v235 op_sel_hi:[0,0,1]
	v_smfmac_f32_16x16x64_f16 v[238:241], v[146:149], a[152:159], v210
	v_fma_mixlo_f16 v233, v231, s42, 0
	ds_write_b16 v205, v232 offset:8704
	s_waitcnt lgkmcnt(5)
	v_smfmac_f32_16x16x64_f16 v[242:245], v[146:149], v[180:187], v210
	ds_read_b128 v[180:183], v199 offset:30720
	ds_read_b128 v[184:187], v199 offset:31744
	ds_write_b16 v205, v235 offset:9248
	ds_write_b16 v205, v233 offset:9792
	v_smfmac_f32_16x16x64_f16 v[238:241], v[150:153], a[184:191], v210
	ds_read_b128 v[230:233], v217
	ds_read_b128 v[234:237], v217
	s_waitcnt lgkmcnt(9)
	v_smfmac_f32_16x16x64_f16 v[242:245], v[150:153], v[188:195], v210
	v_smfmac_f32_16x16x64_f16 v[238:241], v[154:157], a[216:223], v210
	s_waitcnt lgkmcnt(7)
	v_smfmac_f32_16x16x64_f16 v[242:245], v[154:157], v[222:229], v210
	v_smfmac_f32_16x16x64_f16 v[238:241], v[158:161], a[248:255], v210
	s_waitcnt lgkmcnt(4)
	v_smfmac_f32_16x16x64_f16 v[242:245], v[158:161], v[180:187], v210
	s_nop 5
	v_fmac_f32_e32 v238, s40, v239
	s_nop 0
	v_fmac_f32_e32 v242, s40, v243
	v_fmac_f32_e32 v238, s41, v240
	v_fmac_f32_e32 v242, s41, v244
	s_nop 1
	v_permlane32_swap_b32_e32 v238, v242
	v_add_f32_e32 v198, v238, v242
	v_fmac_f32_e32 v247, 0xbe94e4f6, v198
	v_fma_mixlo_f16 v240, v178, v247, v168
	v_fma_f32 v239, v178, v247, v168
	v_fma_mix_f32 v239, v239, 1.0, -v240 op_sel_hi:[0,0,1]
	v_fma_mixlo_f16 v243, v239, s42, 0
	v_fma_mix_f32 v239, v239, s42, -v243 op_sel_hi:[0,0,1]
	v_fma_mixlo_f16 v241, v239, s42, 0
	ds_write_b16 v207, v240 offset:8704
	ds_write_b16 v207, v243 offset:9248
	ds_write_b16 v207, v241 offset:9792
	s_waitcnt lgkmcnt(0)
	s_barrier
	ds_read_b128 v[130:133], v208 offset:8704
	ds_read_b128 v[134:137], v209 offset:8768
	ds_read_b128 v[138:141], v211 offset:8704
	ds_read_b128 v[142:145], v212 offset:8704
	ds_read_b128 v[146:149], v213 offset:8704
	ds_read_b128 v[150:153], v214 offset:8704
	ds_read_b128 v[154:157], v215 offset:8704
	ds_read_b128 v[158:161], v216 offset:8704
	ds_read_b128 v[180:183], v199 offset:0
	ds_read_b128 v[184:187], v199 offset:1024
	ds_read_b128 v[188:191], v199 offset:4096
	ds_read_b128 v[192:195], v199 offset:5120
	ds_read_b128 v[222:225], v199 offset:8192
	s_waitcnt lgkmcnt(6)
	ds_read_b128 v[226:229], v199 offset:9216
	v_smfmac_f32_16x16x64_f16 v[230:233], v[130:133], a[0:7], v210
	ds_read_b128 v[238:241], v217
	ds_read_b128 v[242:245], v217
	v_smfmac_f32_16x16x64_f16 v[234:237], v[130:133], v[18:25], v210
	v_mul_f32_e32 v248, 0x40362960, v173
	v_fmac_f32_e32 v248, 0xc12c1f08, v162
	v_smfmac_f32_16x16x64_f16 v[230:233], v[134:137], a[40:47], v210
	v_fmac_f32_e32 v248, 0x410e80b5, v166
	v_fmac_f32_e32 v248, 0x3e8e8ba3, v179
	v_smfmac_f32_16x16x64_f16 v[234:237], v[134:137], v[34:41], v210
	v_mul_f32_e32 v249, 0x40362960, v172
	v_fmac_f32_e32 v249, 0xc12c1f08, v163
	v_smfmac_f32_16x16x64_f16 v[230:233], v[138:141], a[64:71], v210
	v_fmac_f32_e32 v249, 0x410e80b5, v167
	v_fmac_f32_e32 v249, 0x3e8e8ba3, v196
	v_smfmac_f32_16x16x64_f16 v[234:237], v[138:141], v[42:49], v210
	v_mul_f32_e32 v250, 0x40362960, v175
	v_fmac_f32_e32 v250, 0xc12c1f08, v164
	v_smfmac_f32_16x16x64_f16 v[230:233], v[142:145], a[96:103], v210
	v_fmac_f32_e32 v250, 0x410e80b5, v176
	v_fmac_f32_e32 v250, 0x3e8e8ba3, v197
	v_smfmac_f32_16x16x64_f16 v[234:237], v[142:145], v[58:65], v210
	v_mul_f32_e32 v251, 0x40362960, v174
	v_fmac_f32_e32 v251, 0xc12c1f08, v165
	v_smfmac_f32_16x16x64_f16 v[230:233], v[146:149], a[128:135], v210
	v_fmac_f32_e32 v251, 0x410e80b5, v177
	v_fmac_f32_e32 v251, 0x3e8e8ba3, v198
	v_smfmac_f32_16x16x64_f16 v[234:237], v[146:149], v[74:81], v210
	v_smfmac_f32_16x16x64_f16 v[230:233], v[150:153], a[160:167], v210
	v_smfmac_f32_16x16x64_f16 v[234:237], v[150:153], v[98:105], v210
	v_smfmac_f32_16x16x64_f16 v[230:233], v[154:157], a[192:199], v210
	v_smfmac_f32_16x16x64_f16 v[234:237], v[154:157], v[106:113], v210
	s_waitcnt lgkmcnt(8)
	v_smfmac_f32_16x16x64_f16 v[230:233], v[158:161], a[224:231], v210
	v_smfmac_f32_16x16x64_f16 v[234:237], v[158:161], v[122:129], v210
	s_waitcnt lgkmcnt(1)
	v_smfmac_f32_16x16x64_f16 v[238:241], v[130:133], a[16:23], v210
	s_waitcnt lgkmcnt(0)
	v_smfmac_f32_16x16x64_f16 v[242:245], v[130:133], v[180:187], v210
	ds_read_b128 v[180:183], v199 offset:12288
	ds_read_b128 v[184:187], v199 offset:13312
	v_smfmac_f32_16x16x64_f16 v[238:241], v[134:137], a[48:55], v210
	v_fmac_f32_e32 v230, s40, v231
	v_fmac_f32_e32 v234, s40, v235
	v_smfmac_f32_16x16x64_f16 v[242:245], v[134:137], v[188:195], v210
	ds_read_b128 v[188:191], v199 offset:16384
	ds_read_b128 v[192:195], v199 offset:17408
	v_fmac_f32_e32 v230, s41, v232
	v_fmac_f32_e32 v234, s41, v236
	v_smfmac_f32_16x16x64_f16 v[238:241], v[138:141], a[80:87], v210
	s_nop 0
	v_permlane32_swap_b32_e32 v230, v234
	v_add_f32_e32 v219, v230, v234
	v_smfmac_f32_16x16x64_f16 v[242:245], v[138:141], v[222:229], v210
	ds_read_b128 v[222:225], v199 offset:20480
	ds_read_b128 v[226:229], v199 offset:21504
	v_fmac_f32_e32 v248, 0xbe8c0c4c, v219
	v_fma_mixlo_f16 v232, v178, v248, v171
	v_smfmac_f32_16x16x64_f16 v[238:241], v[142:145], a[112:119], v210
	v_fma_f32 v231, v178, v248, v171
	v_fma_mix_f32 v231, v231, 1.0, -v232 op_sel_hi:[0,0,1]
	s_waitcnt lgkmcnt(4)
	v_smfmac_f32_16x16x64_f16 v[242:245], v[142:145], v[180:187], v210
	ds_read_b128 v[180:183], v199 offset:24576
	ds_read_b128 v[184:187], v199 offset:25600
	v_fma_mixlo_f16 v235, v231, s42, 0
	v_fma_mix_f32 v231, v231, s42, -v235 op_sel_hi:[0,0,1]
	v_smfmac_f32_16x16x64_f16 v[238:241], v[146:149], a[144:151], v210
	v_fma_mixlo_f16 v233, v231, s42, 0
	ds_write_b16 v204, v232
	s_waitcnt lgkmcnt(5)
	v_smfmac_f32_16x16x64_f16 v[242:245], v[146:149], v[188:195], v210
	ds_read_b128 v[188:191], v199 offset:28672
	ds_read_b128 v[192:195], v199 offset:29696
	ds_write_b16 v204, v235 offset:544
	ds_write_b16 v204, v233 offset:1088
	v_smfmac_f32_16x16x64_f16 v[238:241], v[150:153], a[176:183], v210
	ds_read_b128 v[230:233], v217
	ds_read_b128 v[234:237], v217
	s_waitcnt lgkmcnt(9)
	v_smfmac_f32_16x16x64_f16 v[242:245], v[150:153], v[222:229], v210
	ds_read_b128 v[222:225], v199 offset:2048
	ds_read_b128 v[226:229], v199 offset:3072
	v_smfmac_f32_16x16x64_f16 v[238:241], v[154:157], a[208:215], v210
	s_waitcnt lgkmcnt(9)
	v_smfmac_f32_16x16x64_f16 v[242:245], v[154:157], v[180:187], v210
	ds_read_b128 v[180:183], v199 offset:6144
	ds_read_b128 v[184:187], v199 offset:7168
	v_smfmac_f32_16x16x64_f16 v[238:241], v[158:161], a[240:247], v210
	s_waitcnt lgkmcnt(8)
	v_smfmac_f32_16x16x64_f16 v[242:245], v[158:161], v[188:195], v210
	ds_read_b128 v[188:191], v199 offset:10240
	ds_read_b128 v[192:195], v199 offset:11264
	s_waitcnt lgkmcnt(7)
	v_smfmac_f32_16x16x64_f16 v[230:233], v[130:133], a[8:15], v210
	s_waitcnt lgkmcnt(6)
	v_smfmac_f32_16x16x64_f16 v[234:237], v[130:133], v[2:9], v210
	v_smfmac_f32_16x16x64_f16 v[230:233], v[134:137], a[32:39], v210
	v_fmac_f32_e32 v238, s40, v239
	v_fmac_f32_e32 v242, s40, v243
	v_smfmac_f32_16x16x64_f16 v[234:237], v[134:137], v[10:17], v210
	v_fmac_f32_e32 v238, s41, v240
	v_fmac_f32_e32 v242, s41, v244
	v_smfmac_f32_16x16x64_f16 v[230:233], v[138:141], a[72:79], v210
	s_nop 0
	v_permlane32_swap_b32_e32 v238, v242
	v_add_f32_e32 v246, v238, v242
	v_smfmac_f32_16x16x64_f16 v[234:237], v[138:141], v[50:57], v210
	v_fmac_f32_e32 v250, 0xbe8c0c4c, v246
	v_fma_mixlo_f16 v240, v178, v250, v169
	v_smfmac_f32_16x16x64_f16 v[230:233], v[142:145], a[104:111], v210
	v_fma_f32 v239, v178, v250, v169
	v_fma_mix_f32 v239, v239, 1.0, -v240 op_sel_hi:[0,0,1]
	v_smfmac_f32_16x16x64_f16 v[234:237], v[142:145], v[26:33], v210
	v_fma_mixlo_f16 v243, v239, s42, 0
	v_fma_mix_f32 v239, v239, s42, -v243 op_sel_hi:[0,0,1]
	v_smfmac_f32_16x16x64_f16 v[230:233], v[146:149], a[136:143], v210
	v_fma_mixlo_f16 v241, v239, s42, 0
	ds_write_b16 v206, v240
	v_smfmac_f32_16x16x64_f16 v[234:237], v[146:149], v[82:89], v210
	ds_write_b16 v206, v243 offset:544
	ds_write_b16 v206, v241 offset:1088
	v_smfmac_f32_16x16x64_f16 v[230:233], v[150:153], a[168:175], v210
	ds_read_b128 v[238:241], v217
	ds_read_b128 v[242:245], v217
	v_smfmac_f32_16x16x64_f16 v[234:237], v[150:153], v[66:73], v210
	v_smfmac_f32_16x16x64_f16 v[230:233], v[154:157], a[200:207], v210
	v_smfmac_f32_16x16x64_f16 v[234:237], v[154:157], v[114:121], v210
	v_smfmac_f32_16x16x64_f16 v[230:233], v[158:161], a[232:239], v210
	v_smfmac_f32_16x16x64_f16 v[234:237], v[158:161], v[90:97], v210
	s_waitcnt lgkmcnt(1)
	v_smfmac_f32_16x16x64_f16 v[238:241], v[130:133], a[24:31], v210
	s_waitcnt lgkmcnt(0)
	v_smfmac_f32_16x16x64_f16 v[242:245], v[130:133], v[222:229], v210
	ds_read_b128 v[222:225], v199 offset:14336
	ds_read_b128 v[226:229], v199 offset:15360
	v_smfmac_f32_16x16x64_f16 v[238:241], v[134:137], a[56:63], v210
	v_fmac_f32_e32 v230, s40, v231
	v_fmac_f32_e32 v234, s40, v235
	v_smfmac_f32_16x16x64_f16 v[242:245], v[134:137], v[180:187], v210
	ds_read_b128 v[180:183], v199 offset:18432
	ds_read_b128 v[184:187], v199 offset:19456
	v_fmac_f32_e32 v230, s41, v232
	v_fmac_f32_e32 v234, s41, v236
	v_smfmac_f32_16x16x64_f16 v[238:241], v[138:141], a[88:95], v210
	s_nop 0
	v_permlane32_swap_b32_e32 v230, v234
	v_add_f32_e32 v220, v230, v234
	v_smfmac_f32_16x16x64_f16 v[242:245], v[138:141], v[188:195], v210
	ds_read_b128 v[188:191], v199 offset:22528
	ds_read_b128 v[192:195], v199 offset:23552
	v_fmac_f32_e32 v249, 0xbe8c0c4c, v220
	v_fma_mixlo_f16 v232, v178, v249, v170
	v_smfmac_f32_16x16x64_f16 v[238:241], v[142:145], a[120:127], v210
	v_fma_f32 v231, v178, v249, v170
	v_fma_mix_f32 v231, v231, 1.0, -v232 op_sel_hi:[0,0,1]
	s_waitcnt lgkmcnt(4)
	v_smfmac_f32_16x16x64_f16 v[242:245], v[142:145], v[222:229], v210
	ds_read_b128 v[222:225], v199 offset:26624
	ds_read_b128 v[226:229], v199 offset:27648
	v_fma_mixlo_f16 v235, v231, s42, 0
	v_fma_mix_f32 v231, v231, s42, -v235 op_sel_hi:[0,0,1]
	v_smfmac_f32_16x16x64_f16 v[238:241], v[146:149], a[152:159], v210
	v_fma_mixlo_f16 v233, v231, s42, 0
	ds_write_b16 v205, v232
	s_waitcnt lgkmcnt(5)
	v_smfmac_f32_16x16x64_f16 v[242:245], v[146:149], v[180:187], v210
	ds_read_b128 v[180:183], v199 offset:30720
	ds_read_b128 v[184:187], v199 offset:31744
	ds_write_b16 v205, v235 offset:544
	ds_write_b16 v205, v233 offset:1088
	v_smfmac_f32_16x16x64_f16 v[238:241], v[150:153], a[184:191], v210
	ds_read_b128 v[230:233], v217
	ds_read_b128 v[234:237], v217
	s_waitcnt lgkmcnt(9)
	v_smfmac_f32_16x16x64_f16 v[242:245], v[150:153], v[188:195], v210
	v_smfmac_f32_16x16x64_f16 v[238:241], v[154:157], a[216:223], v210
	s_waitcnt lgkmcnt(7)
	v_smfmac_f32_16x16x64_f16 v[242:245], v[154:157], v[222:229], v210
	v_smfmac_f32_16x16x64_f16 v[238:241], v[158:161], a[248:255], v210
	s_waitcnt lgkmcnt(4)
	v_smfmac_f32_16x16x64_f16 v[242:245], v[158:161], v[180:187], v210
	s_nop 5
	v_fmac_f32_e32 v238, s40, v239
	s_nop 0
	v_fmac_f32_e32 v242, s40, v243
	v_fmac_f32_e32 v238, s41, v240
	v_fmac_f32_e32 v242, s41, v244
	s_nop 1
	v_permlane32_swap_b32_e32 v238, v242
	v_add_f32_e32 v247, v238, v242
	v_fmac_f32_e32 v251, 0xbe8c0c4c, v247
	v_fma_mixlo_f16 v240, v178, v251, v168
	v_fma_f32 v239, v178, v251, v168
	v_fma_mix_f32 v239, v239, 1.0, -v240 op_sel_hi:[0,0,1]
	v_fma_mixlo_f16 v243, v239, s42, 0
	v_fma_mix_f32 v239, v239, s42, -v243 op_sel_hi:[0,0,1]
	v_fma_mixlo_f16 v241, v239, s42, 0
	ds_write_b16 v207, v240
	ds_write_b16 v207, v243 offset:544
	ds_write_b16 v207, v241 offset:1088
	s_waitcnt lgkmcnt(0)
	s_barrier
	ds_read_b128 v[130:133], v208
	ds_read_b128 v[134:137], v209 offset:64
	ds_read_b128 v[138:141], v211
	ds_read_b128 v[142:145], v212
	ds_read_b128 v[146:149], v213
	ds_read_b128 v[150:153], v214
	ds_read_b128 v[154:157], v215
	ds_read_b128 v[158:161], v216
	ds_read_b128 v[180:183], v199 offset:0
	ds_read_b128 v[184:187], v199 offset:1024
	ds_read_b128 v[188:191], v199 offset:4096
	ds_read_b128 v[192:195], v199 offset:5120
	ds_read_b128 v[222:225], v199 offset:8192
	s_waitcnt lgkmcnt(6)
	ds_read_b128 v[226:229], v199 offset:9216
	v_smfmac_f32_16x16x64_f16 v[230:233], v[130:133], a[0:7], v210
	ds_read_b128 v[238:241], v217
	ds_read_b128 v[242:245], v217
	v_smfmac_f32_16x16x64_f16 v[234:237], v[130:133], v[18:25], v210
	v_mul_f32_e32 v252, 0x3dbaaaab, v173
	v_fmac_f32_e32 v252, 0x3ee6024d, v166
	v_smfmac_f32_16x16x64_f16 v[230:233], v[134:137], a[40:47], v210
	v_fmac_f32_e32 v252, 0x3f26aaab, v179
	v_fmac_f32_e32 v252, 0xbea50e7e, v219
	v_smfmac_f32_16x16x64_f16 v[234:237], v[134:137], v[34:41], v210
	v_mul_f32_e32 v253, 0x3dbaaaab, v172
	v_fmac_f32_e32 v253, 0x3ee6024d, v167
	v_smfmac_f32_16x16x64_f16 v[230:233], v[138:141], a[64:71], v210
	v_fmac_f32_e32 v253, 0x3f26aaab, v196
	v_fmac_f32_e32 v253, 0xbea50e7e, v220
	v_smfmac_f32_16x16x64_f16 v[234:237], v[138:141], v[42:49], v210
	v_mul_f32_e32 v254, 0x3dbaaaab, v175
	v_fmac_f32_e32 v254, 0x3ee6024d, v176
	v_smfmac_f32_16x16x64_f16 v[230:233], v[142:145], a[96:103], v210
	v_fmac_f32_e32 v254, 0x3f26aaab, v197
	v_fmac_f32_e32 v254, 0xbea50e7e, v246
	v_smfmac_f32_16x16x64_f16 v[234:237], v[142:145], v[58:65], v210
	v_mul_f32_e32 v255, 0x3dbaaaab, v174
	v_fmac_f32_e32 v255, 0x3ee6024d, v177
	v_smfmac_f32_16x16x64_f16 v[230:233], v[146:149], a[128:135], v210
	v_fmac_f32_e32 v255, 0x3f26aaab, v198
	v_fmac_f32_e32 v255, 0xbea50e7e, v247
	v_smfmac_f32_16x16x64_f16 v[234:237], v[146:149], v[74:81], v210
	v_smfmac_f32_16x16x64_f16 v[230:233], v[150:153], a[160:167], v210
	v_smfmac_f32_16x16x64_f16 v[234:237], v[150:153], v[98:105], v210
	v_smfmac_f32_16x16x64_f16 v[230:233], v[154:157], a[192:199], v210
	v_smfmac_f32_16x16x64_f16 v[234:237], v[154:157], v[106:113], v210
	s_waitcnt lgkmcnt(8)
	v_smfmac_f32_16x16x64_f16 v[230:233], v[158:161], a[224:231], v210
	v_smfmac_f32_16x16x64_f16 v[234:237], v[158:161], v[122:129], v210
	s_waitcnt lgkmcnt(1)
	v_smfmac_f32_16x16x64_f16 v[238:241], v[130:133], a[16:23], v210
	s_waitcnt lgkmcnt(0)
	v_smfmac_f32_16x16x64_f16 v[242:245], v[130:133], v[180:187], v210
	ds_read_b128 v[180:183], v199 offset:12288
	ds_read_b128 v[184:187], v199 offset:13312
	v_smfmac_f32_16x16x64_f16 v[238:241], v[134:137], a[48:55], v210
	v_fmac_f32_e32 v230, s40, v231
	v_fmac_f32_e32 v234, s40, v235
	v_smfmac_f32_16x16x64_f16 v[242:245], v[134:137], v[188:195], v210
	ds_read_b128 v[188:191], v199 offset:16384
	ds_read_b128 v[192:195], v199 offset:17408
	v_fmac_f32_e32 v230, s41, v232
	v_fmac_f32_e32 v234, s41, v236
	v_smfmac_f32_16x16x64_f16 v[238:241], v[138:141], a[80:87], v210
	s_nop 0
	v_permlane32_swap_b32_e32 v230, v234
	v_add_f32_e32 v248, v230, v234
	v_smfmac_f32_16x16x64_f16 v[242:245], v[138:141], v[222:229], v210
	ds_read_b128 v[222:225], v199 offset:20480
	ds_read_b128 v[226:229], v199 offset:21504
	v_fmac_f32_e32 v252, 0x3e061862, v248
	v_mov_b32_e32 v236, v252
	v_smfmac_f32_16x16x64_f16 v[238:241], v[142:145], a[112:119], v210
	v_fma_mixlo_f16 v232, v178, v236, v171
	v_fma_f32 v252, v178, v236, v171
	s_waitcnt lgkmcnt(4)
	v_smfmac_f32_16x16x64_f16 v[242:245], v[142:145], v[180:187], v210
	ds_read_b128 v[180:183], v199 offset:24576
	ds_read_b128 v[184:187], v199 offset:25600
	v_fma_mix_f32 v231, v252, 1.0, -v232 op_sel_hi:[0,0,1]
	v_fma_mixlo_f16 v235, v231, s42, 0
	v_smfmac_f32_16x16x64_f16 v[238:241], v[146:149], a[144:151], v210
	v_fma_mix_f32 v231, v231, s42, -v235 op_sel_hi:[0,0,1]
	v_fma_mixlo_f16 v233, v231, s42, 0
	s_waitcnt lgkmcnt(4)
	v_smfmac_f32_16x16x64_f16 v[242:245], v[146:149], v[188:195], v210
	ds_read_b128 v[188:191], v199 offset:28672
	ds_read_b128 v[192:195], v199 offset:29696
	ds_write_b16 v204, v232 offset:8704
	ds_write_b16 v204, v235 offset:9248
	v_smfmac_f32_16x16x64_f16 v[238:241], v[150:153], a[176:183], v210
	ds_write_b16 v204, v233 offset:9792
	ds_read_b128 v[230:233], v217
	s_waitcnt lgkmcnt(8)
	v_smfmac_f32_16x16x64_f16 v[242:245], v[150:153], v[222:229], v210
	ds_read_b128 v[222:225], v199 offset:2048
	ds_read_b128 v[226:229], v199 offset:3072
	ds_read_b128 v[234:237], v217
	v_smfmac_f32_16x16x64_f16 v[238:241], v[154:157], a[208:215], v210
	s_waitcnt lgkmcnt(9)
	v_smfmac_f32_16x16x64_f16 v[242:245], v[154:157], v[180:187], v210
	ds_read_b128 v[180:183], v199 offset:6144
	ds_read_b128 v[184:187], v199 offset:7168
	v_smfmac_f32_16x16x64_f16 v[238:241], v[158:161], a[240:247], v210
	s_waitcnt lgkmcnt(9)
	v_smfmac_f32_16x16x64_f16 v[242:245], v[158:161], v[188:195], v210
	ds_read_b128 v[188:191], v199 offset:10240
	ds_read_b128 v[192:195], v199 offset:11264
	s_waitcnt lgkmcnt(7)
	v_smfmac_f32_16x16x64_f16 v[230:233], v[130:133], a[8:15], v210
	s_waitcnt lgkmcnt(4)
	v_smfmac_f32_16x16x64_f16 v[234:237], v[130:133], v[2:9], v210
	v_smfmac_f32_16x16x64_f16 v[230:233], v[134:137], a[32:39], v210
	v_fmac_f32_e32 v238, s40, v239
	v_fmac_f32_e32 v242, s40, v243
	v_smfmac_f32_16x16x64_f16 v[234:237], v[134:137], v[10:17], v210
	v_fmac_f32_e32 v238, s41, v240
	v_fmac_f32_e32 v242, s41, v244
	v_smfmac_f32_16x16x64_f16 v[230:233], v[138:141], a[72:79], v210
	s_nop 0
	v_permlane32_swap_b32_e32 v238, v242
	v_add_f32_e32 v250, v238, v242
	v_smfmac_f32_16x16x64_f16 v[234:237], v[138:141], v[50:57], v210
	v_fmac_f32_e32 v254, 0x3e061862, v250
	v_mov_b32_e32 v244, v254
	v_smfmac_f32_16x16x64_f16 v[230:233], v[142:145], a[104:111], v210
	v_fma_mixlo_f16 v240, v178, v244, v169
	v_fma_f32 v254, v178, v244, v169
	v_smfmac_f32_16x16x64_f16 v[234:237], v[142:145], v[26:33], v210
	v_fma_mix_f32 v239, v254, 1.0, -v240 op_sel_hi:[0,0,1]
	v_fma_mixlo_f16 v243, v239, s42, 0
	v_smfmac_f32_16x16x64_f16 v[230:233], v[146:149], a[136:143], v210
	v_fma_mix_f32 v239, v239, s42, -v243 op_sel_hi:[0,0,1]
	v_fma_mixlo_f16 v241, v239, s42, 0
	v_smfmac_f32_16x16x64_f16 v[234:237], v[146:149], v[82:89], v210
	ds_write_b16 v206, v240 offset:8704
	ds_write_b16 v206, v243 offset:9248
	v_smfmac_f32_16x16x64_f16 v[230:233], v[150:153], a[168:175], v210
	ds_write_b16 v206, v241 offset:9792
	ds_read_b128 v[238:241], v217
	v_smfmac_f32_16x16x64_f16 v[234:237], v[150:153], v[66:73], v210
	ds_read_b128 v[242:245], v217
	v_smfmac_f32_16x16x64_f16 v[230:233], v[154:157], a[200:207], v210
	v_smfmac_f32_16x16x64_f16 v[234:237], v[154:157], v[114:121], v210
	v_smfmac_f32_16x16x64_f16 v[230:233], v[158:161], a[232:239], v210
	v_smfmac_f32_16x16x64_f16 v[234:237], v[158:161], v[90:97], v210
	s_waitcnt lgkmcnt(1)
	v_smfmac_f32_16x16x64_f16 v[238:241], v[130:133], a[24:31], v210
	s_waitcnt lgkmcnt(0)
	v_smfmac_f32_16x16x64_f16 v[242:245], v[130:133], v[222:229], v210
	ds_read_b128 v[222:225], v199 offset:14336
	ds_read_b128 v[226:229], v199 offset:15360
	v_smfmac_f32_16x16x64_f16 v[238:241], v[134:137], a[56:63], v210
	v_fmac_f32_e32 v230, s40, v231
	v_fmac_f32_e32 v234, s40, v235
	v_smfmac_f32_16x16x64_f16 v[242:245], v[134:137], v[180:187], v210
	ds_read_b128 v[180:183], v199 offset:18432
	ds_read_b128 v[184:187], v199 offset:19456
	v_fmac_f32_e32 v230, s41, v232
	v_fmac_f32_e32 v234, s41, v236
	v_smfmac_f32_16x16x64_f16 v[238:241], v[138:141], a[88:95], v210
	s_nop 0
	v_permlane32_swap_b32_e32 v230, v234
	v_add_f32_e32 v249, v230, v234
	v_smfmac_f32_16x16x64_f16 v[242:245], v[138:141], v[188:195], v210
	ds_read_b128 v[188:191], v199 offset:22528
	ds_read_b128 v[192:195], v199 offset:23552
	v_fmac_f32_e32 v253, 0x3e061862, v249
	v_mov_b32_e32 v236, v253
	v_smfmac_f32_16x16x64_f16 v[238:241], v[142:145], a[120:127], v210
	v_fma_mixlo_f16 v232, v178, v236, v170
	v_fma_f32 v253, v178, v236, v170
	s_waitcnt lgkmcnt(4)
	v_smfmac_f32_16x16x64_f16 v[242:245], v[142:145], v[222:229], v210
	ds_read_b128 v[222:225], v199 offset:26624
	ds_read_b128 v[226:229], v199 offset:27648
	v_fma_mix_f32 v231, v253, 1.0, -v232 op_sel_hi:[0,0,1]
	v_fma_mixlo_f16 v235, v231, s42, 0
	v_smfmac_f32_16x16x64_f16 v[238:241], v[146:149], a[152:159], v210
	v_fma_mix_f32 v231, v231, s42, -v235 op_sel_hi:[0,0,1]
	v_fma_mixlo_f16 v233, v231, s42, 0
	s_waitcnt lgkmcnt(4)
	v_smfmac_f32_16x16x64_f16 v[242:245], v[146:149], v[180:187], v210
	ds_read_b128 v[180:183], v199 offset:30720
	ds_read_b128 v[184:187], v199 offset:31744
	ds_write_b16 v205, v232 offset:8704
	ds_write_b16 v205, v235 offset:9248
	v_smfmac_f32_16x16x64_f16 v[238:241], v[150:153], a[184:191], v210
	ds_write_b16 v205, v233 offset:9792
	ds_read_b128 v[230:233], v217
	s_waitcnt lgkmcnt(8)
	v_smfmac_f32_16x16x64_f16 v[242:245], v[150:153], v[188:195], v210
	ds_read_b128 v[234:237], v217
	v_smfmac_f32_16x16x64_f16 v[238:241], v[154:157], a[216:223], v210
	s_waitcnt lgkmcnt(7)
	v_smfmac_f32_16x16x64_f16 v[242:245], v[154:157], v[222:229], v210
	v_smfmac_f32_16x16x64_f16 v[238:241], v[158:161], a[248:255], v210
	s_waitcnt lgkmcnt(5)
	v_smfmac_f32_16x16x64_f16 v[242:245], v[158:161], v[180:187], v210
	s_nop 5
	v_fmac_f32_e32 v238, s40, v239
	s_nop 0
	v_fmac_f32_e32 v242, s40, v243
	v_fmac_f32_e32 v238, s41, v240
	v_fmac_f32_e32 v242, s41, v244
	s_nop 1
	v_permlane32_swap_b32_e32 v238, v242
	v_add_f32_e32 v251, v238, v242
	v_fmac_f32_e32 v255, 0x3e061862, v251
	v_mov_b32_e32 v244, v255
	v_fma_mixlo_f16 v240, v178, v244, v168
	v_fma_f32 v255, v178, v244, v168
	v_fma_mix_f32 v239, v255, 1.0, -v240 op_sel_hi:[0,0,1]
	v_fma_mixlo_f16 v243, v239, s42, 0
	v_fma_mix_f32 v239, v239, s42, -v243 op_sel_hi:[0,0,1]
	v_fma_mixlo_f16 v241, v239, s42, 0
	ds_write_b16 v207, v240 offset:8704
	ds_write_b16 v207, v243 offset:9248
	ds_write_b16 v207, v241 offset:9792
	s_waitcnt lgkmcnt(0)
	s_barrier
	ds_read_b128 v[130:133], v208 offset:8704
	ds_read_b128 v[134:137], v209 offset:8768
	ds_read_b128 v[138:141], v211 offset:8704
	ds_read_b128 v[142:145], v212 offset:8704
	ds_read_b128 v[146:149], v213 offset:8704
	ds_read_b128 v[150:153], v214 offset:8704
	ds_read_b128 v[154:157], v215 offset:8704
	ds_read_b128 v[158:161], v216 offset:8704
	ds_read_b128 v[180:183], v199 offset:0
	ds_read_b128 v[184:187], v199 offset:1024
	ds_read_b128 v[188:191], v199 offset:4096
	ds_read_b128 v[192:195], v199 offset:5120
	ds_read_b128 v[222:225], v199 offset:8192
	s_waitcnt lgkmcnt(6)
	ds_read_b128 v[226:229], v199 offset:9216
	v_smfmac_f32_16x16x64_f16 v[230:233], v[130:133], a[0:7], v210
	ds_read_b128 v[238:241], v217
	ds_read_b128 v[242:245], v217
	v_smfmac_f32_16x16x64_f16 v[234:237], v[130:133], v[18:25], v210
	v_mul_f32_e32 v162, 0x3aa1907f, v173
	v_fmac_f32_e32 v162, 0xbb8b5ad3, v166
	v_smfmac_f32_16x16x64_f16 v[230:233], v[134:137], a[40:47], v210
	v_fmac_f32_e32 v162, 0x3d177777, v179
	v_fmac_f32_e32 v162, 0xbd50568f, v219
	v_smfmac_f32_16x16x64_f16 v[234:237], v[134:137], v[34:41], v210
	v_fmac_f32_e32 v162, 0x3d2ba454, v248
	v_mul_f32_e32 v163, 0x3aa1907f, v172
	v_smfmac_f32_16x16x64_f16 v[230:233], v[138:141], a[64:71], v210
	v_fmac_f32_e32 v163, 0xbb8b5ad3, v167
	v_fmac_f32_e32 v163, 0x3d177777, v196
	v_smfmac_f32_16x16x64_f16 v[234:237], v[138:141], v[42:49], v210
	v_fmac_f32_e32 v163, 0xbd50568f, v220
	v_fmac_f32_e32 v163, 0x3d2ba454, v249
	v_smfmac_f32_16x16x64_f16 v[230:233], v[142:145], a[96:103], v210
	v_mul_f32_e32 v164, 0x3aa1907f, v175
	v_fmac_f32_e32 v164, 0xbb8b5ad3, v176
	v_smfmac_f32_16x16x64_f16 v[234:237], v[142:145], v[58:65], v210
	v_fmac_f32_e32 v164, 0x3d177777, v197
	v_fmac_f32_e32 v164, 0xbd50568f, v246
	v_smfmac_f32_16x16x64_f16 v[230:233], v[146:149], a[128:135], v210
	v_fmac_f32_e32 v164, 0x3d2ba454, v250
	v_mul_f32_e32 v165, 0x3aa1907f, v174
	v_smfmac_f32_16x16x64_f16 v[234:237], v[146:149], v[74:81], v210
	v_fmac_f32_e32 v165, 0xbb8b5ad3, v177
	v_fmac_f32_e32 v165, 0x3d177777, v198
	v_smfmac_f32_16x16x64_f16 v[230:233], v[150:153], a[160:167], v210
	v_fmac_f32_e32 v165, 0xbd50568f, v247
	v_fmac_f32_e32 v165, 0x3d2ba454, v251
	v_smfmac_f32_16x16x64_f16 v[234:237], v[150:153], v[98:105], v210
	v_max_f32_e64 v179, |v171|, |v252|
	v_mov_b32_e32 v248, 0x358637bd
	v_smfmac_f32_16x16x64_f16 v[230:233], v[154:157], a[192:199], v210
	v_fmac_f32_e32 v248, 0x3a83126f, v179
	v_rcp_f32_e32 v179, v248
	v_smfmac_f32_16x16x64_f16 v[234:237], v[154:157], v[106:113], v210
	v_max_f32_e64 v196, |v170|, |v253|
	v_mov_b32_e32 v249, 0x358637bd
	s_waitcnt lgkmcnt(8)
	v_smfmac_f32_16x16x64_f16 v[230:233], v[158:161], a[224:231], v210
	v_fmac_f32_e32 v249, 0x3a83126f, v196
	v_rcp_f32_e32 v196, v249
	v_smfmac_f32_16x16x64_f16 v[234:237], v[158:161], v[122:129], v210
	v_max_f32_e64 v197, |v169|, |v254|
	v_mov_b32_e32 v250, 0x358637bd
	v_fmac_f32_e32 v250, 0x3a83126f, v197
	v_rcp_f32_e32 v197, v250
	v_max_f32_e64 v198, |v168|, |v255|
	v_mov_b32_e32 v251, 0x358637bd
	v_fmac_f32_e32 v251, 0x3a83126f, v198
	v_rcp_f32_e32 v198, v251
	s_waitcnt lgkmcnt(1)
	v_smfmac_f32_16x16x64_f16 v[238:241], v[130:133], a[16:23], v210
	s_waitcnt lgkmcnt(0)
	v_smfmac_f32_16x16x64_f16 v[242:245], v[130:133], v[180:187], v210
	ds_read_b128 v[180:183], v199 offset:12288
	ds_read_b128 v[184:187], v199 offset:13312
	v_smfmac_f32_16x16x64_f16 v[238:241], v[134:137], a[48:55], v210
	v_fmac_f32_e32 v230, s40, v231
	v_fmac_f32_e32 v234, s40, v235
	v_smfmac_f32_16x16x64_f16 v[242:245], v[134:137], v[188:195], v210
	ds_read_b128 v[188:191], v199 offset:16384
	ds_read_b128 v[192:195], v199 offset:17408
	v_fmac_f32_e32 v230, s41, v232
	v_fmac_f32_e32 v234, s41, v236
	v_smfmac_f32_16x16x64_f16 v[238:241], v[138:141], a[80:87], v210
	s_nop 0
	v_permlane32_swap_b32_e32 v230, v234
	v_add_f32_e32 v166, v230, v234
	v_smfmac_f32_16x16x64_f16 v[242:245], v[138:141], v[222:229], v210
	ds_read_b128 v[222:225], v199 offset:20480
	ds_read_b128 v[226:229], v199 offset:21504
	v_fmac_f32_e32 v162, 0xbccccccd, v166
	v_mul_f32_e32 v231, v178, v162
	v_smfmac_f32_16x16x64_f16 v[238:241], v[142:145], a[112:119], v210
	v_mul_f32_e32 v231, v231, v179
	v_mul_f32_e32 v219, v231, v231
	s_waitcnt lgkmcnt(4)
	v_smfmac_f32_16x16x64_f16 v[242:245], v[142:145], v[180:187], v210
	ds_read_b128 v[180:183], v199 offset:24576
	ds_read_b128 v[184:187], v199 offset:25600
	ds_read_b128 v[230:233], v217
	ds_read_b128 v[234:237], v217
	v_smfmac_f32_16x16x64_f16 v[238:241], v[146:149], a[144:151], v210
	s_waitcnt lgkmcnt(6)
	v_smfmac_f32_16x16x64_f16 v[242:245], v[146:149], v[188:195], v210
	ds_read_b128 v[188:191], v199 offset:28672
	ds_read_b128 v[192:195], v199 offset:29696
	v_smfmac_f32_16x16x64_f16 v[238:241], v[150:153], a[176:183], v210
	s_waitcnt lgkmcnt(6)
	v_smfmac_f32_16x16x64_f16 v[242:245], v[150:153], v[222:229], v210
	ds_read_b128 v[222:225], v199 offset:2048
	ds_read_b128 v[226:229], v199 offset:3072
	v_smfmac_f32_16x16x64_f16 v[238:241], v[154:157], a[208:215], v210
	s_waitcnt lgkmcnt(6)
	v_smfmac_f32_16x16x64_f16 v[242:245], v[154:157], v[180:187], v210
	ds_read_b128 v[180:183], v199 offset:6144
	ds_read_b128 v[184:187], v199 offset:7168
	v_smfmac_f32_16x16x64_f16 v[238:241], v[158:161], a[240:247], v210
	s_waitcnt lgkmcnt(4)
	v_smfmac_f32_16x16x64_f16 v[242:245], v[158:161], v[188:195], v210
	ds_read_b128 v[188:191], v199 offset:10240
	ds_read_b128 v[192:195], v199 offset:11264
	v_smfmac_f32_16x16x64_f16 v[230:233], v[130:133], a[8:15], v210
	v_smfmac_f32_16x16x64_f16 v[234:237], v[130:133], v[2:9], v210
	v_smfmac_f32_16x16x64_f16 v[230:233], v[134:137], a[32:39], v210
	v_fmac_f32_e32 v238, s40, v239
	v_fmac_f32_e32 v242, s40, v243
	v_smfmac_f32_16x16x64_f16 v[234:237], v[134:137], v[10:17], v210
	v_fmac_f32_e32 v238, s41, v240
	v_fmac_f32_e32 v242, s41, v244
	v_smfmac_f32_16x16x64_f16 v[230:233], v[138:141], a[72:79], v210
	s_nop 0
	v_permlane32_swap_b32_e32 v238, v242
	v_add_f32_e32 v176, v238, v242
	v_smfmac_f32_16x16x64_f16 v[234:237], v[138:141], v[50:57], v210
	v_fmac_f32_e32 v164, 0xbccccccd, v176
	v_mul_f32_e32 v239, v178, v164
	v_smfmac_f32_16x16x64_f16 v[230:233], v[142:145], a[104:111], v210
	v_mul_f32_e32 v239, v239, v197
	v_fmac_f32_e32 v219, v239, v239
	v_smfmac_f32_16x16x64_f16 v[234:237], v[142:145], v[26:33], v210
	ds_read_b128 v[238:241], v217
	ds_read_b128 v[242:245], v217
	v_smfmac_f32_16x16x64_f16 v[230:233], v[146:149], a[136:143], v210
	v_smfmac_f32_16x16x64_f16 v[234:237], v[146:149], v[82:89], v210
	v_smfmac_f32_16x16x64_f16 v[230:233], v[150:153], a[168:175], v210
	v_smfmac_f32_16x16x64_f16 v[234:237], v[150:153], v[66:73], v210
	v_smfmac_f32_16x16x64_f16 v[230:233], v[154:157], a[200:207], v210
	v_smfmac_f32_16x16x64_f16 v[234:237], v[154:157], v[114:121], v210
	v_smfmac_f32_16x16x64_f16 v[230:233], v[158:161], a[232:239], v210
	v_smfmac_f32_16x16x64_f16 v[234:237], v[158:161], v[90:97], v210
	s_waitcnt lgkmcnt(1)
	v_smfmac_f32_16x16x64_f16 v[238:241], v[130:133], a[24:31], v210
	s_waitcnt lgkmcnt(0)
	v_smfmac_f32_16x16x64_f16 v[242:245], v[130:133], v[222:229], v210
	ds_read_b128 v[222:225], v199 offset:14336
	ds_read_b128 v[226:229], v199 offset:15360
	v_smfmac_f32_16x16x64_f16 v[238:241], v[134:137], a[56:63], v210
	v_fmac_f32_e32 v230, s40, v231
	v_fmac_f32_e32 v234, s40, v235
	v_smfmac_f32_16x16x64_f16 v[242:245], v[134:137], v[180:187], v210
	ds_read_b128 v[180:183], v199 offset:18432
	ds_read_b128 v[184:187], v199 offset:19456
	v_fmac_f32_e32 v230, s41, v232
	v_fmac_f32_e32 v234, s41, v236
	v_smfmac_f32_16x16x64_f16 v[238:241], v[138:141], a[88:95], v210
	s_nop 0
	v_permlane32_swap_b32_e32 v230, v234
	v_add_f32_e32 v167, v230, v234
	v_smfmac_f32_16x16x64_f16 v[242:245], v[138:141], v[188:195], v210
	ds_read_b128 v[188:191], v199 offset:22528
	ds_read_b128 v[192:195], v199 offset:23552
	v_fmac_f32_e32 v163, 0xbccccccd, v167
	v_mul_f32_e32 v231, v178, v163
	v_smfmac_f32_16x16x64_f16 v[238:241], v[142:145], a[120:127], v210
	v_mul_f32_e32 v231, v231, v196
	v_fmac_f32_e32 v219, v231, v231
	s_waitcnt lgkmcnt(4)
	v_smfmac_f32_16x16x64_f16 v[242:245], v[142:145], v[222:229], v210
	ds_read_b128 v[222:225], v199 offset:26624
	ds_read_b128 v[226:229], v199 offset:27648
	ds_read_b128 v[230:233], v217
	ds_read_b128 v[234:237], v217
	v_smfmac_f32_16x16x64_f16 v[238:241], v[146:149], a[152:159], v210
	s_waitcnt lgkmcnt(6)
	v_smfmac_f32_16x16x64_f16 v[242:245], v[146:149], v[180:187], v210
	ds_read_b128 v[180:183], v199 offset:30720
	ds_read_b128 v[184:187], v199 offset:31744
	v_smfmac_f32_16x16x64_f16 v[238:241], v[150:153], a[184:191], v210
	s_waitcnt lgkmcnt(6)
	v_smfmac_f32_16x16x64_f16 v[242:245], v[150:153], v[188:195], v210
	v_smfmac_f32_16x16x64_f16 v[238:241], v[154:157], a[216:223], v210
	s_waitcnt lgkmcnt(4)
	v_smfmac_f32_16x16x64_f16 v[242:245], v[154:157], v[222:229], v210
	v_smfmac_f32_16x16x64_f16 v[238:241], v[158:161], a[248:255], v210
	s_waitcnt lgkmcnt(0)
	v_smfmac_f32_16x16x64_f16 v[242:245], v[158:161], v[180:187], v210
	s_nop 5
	v_fmac_f32_e32 v238, s40, v239
	s_nop 0
	v_fmac_f32_e32 v242, s40, v243
	v_fmac_f32_e32 v238, s41, v240
	v_fmac_f32_e32 v242, s41, v244
	s_nop 1
	v_permlane32_swap_b32_e32 v238, v242
	v_add_f32_e32 v177, v238, v242
	v_fmac_f32_e32 v165, 0xbccccccd, v177
	v_mul_f32_e32 v239, v178, v165
	v_mul_f32_e32 v239, v239, v198
	v_fmac_f32_e32 v219, v239, v239
	s_nop 1
	v_add_f32_dpp v238, v219, v219 quad_perm:[1,0,3,2] row_mask:0xf bank_mask:0xf bound_ctrl:1
	s_nop 1
	v_add_f32_dpp v238, v238, v238 quad_perm:[2,3,0,1] row_mask:0xf bank_mask:0xf bound_ctrl:1
	s_nop 1
	v_add_f32_dpp v238, v238, v238 row_half_mirror row_mask:0xf bank_mask:0xf bound_ctrl:1
	s_nop 1
	v_add_f32_dpp v238, v238, v238 row_mirror row_mask:0xf bank_mask:0xf bound_ctrl:1
	v_mov_b32_e32 v239, v238
	s_nop 1
	v_permlane32_swap_b32_e32 v238, v239
	v_add_f32_e32 v238, v238, v239
	v_lshl_add_u32 v240, s29, 6, v218
	v_lshlrev_b32_e32 v241, 3, v201
	v_or_b32_e32 v241, 0x24400, v241
	v_lshl_add_u32 v241, s29, 6, v241
	s_and_saveexec_b64 s[2:3], s[4:5]
	ds_write_b32 v240, v238
	s_or_b64 exec, exec, s[2:3]
	s_waitcnt lgkmcnt(0)
	s_barrier
	ds_read2_b32 v[130:131], v241 offset1:4
	ds_read2_b32 v[132:133], v241 offset0:8 offset1:12
	s_waitcnt lgkmcnt(1)
	v_add_f32_e32 v238, v130, v131
	s_waitcnt lgkmcnt(0)
	v_add_f32_e32 v238, v238, v132
	v_add_f32_e32 v238, v238, v133
	v_mul_f32_e32 v238, 0x3b000000, v238
	v_max_f32_e32 v238, 0xda24260, v238
	v_sqrt_f32_e32 v238, v238
	s_nop 0
	v_cmp_ngt_f32_e64 s[2:3], 1.0, v238
	v_cmp_gt_f32_e32 vcc, 1.0, v238
	v_log_f32_e32 v239, v238
	v_mul_f32_e32 v241, 0x44000000, v178
	s_and_saveexec_b64 s[26:27], vcc
	v_add_f32_e32 v221, v221, v241
	v_mov_b32_e32 v171, v252
	v_mov_b32_e32 v173, v166
	v_mov_b32_e32 v170, v253
	v_mov_b32_e32 v172, v167
	v_mov_b32_e32 v169, v254
	v_mov_b32_e32 v175, v176
	v_mov_b32_e32 v168, v255
	v_mov_b32_e32 v174, v177
	s_or_b64 exec, exec, s[26:27]
	v_mov_b32_e32 v240, 0x41200000
	s_nop 0
	v_cndmask_b32_e64 v240, v240, 1.0, s[22:23]
	s_xor_b32 s29, s29, 1
	s_add_i32 s30, s30, 1
	v_mul_f32_e32 v239, 0xbe4ccccd, v239
	v_exp_f32_e32 v239, v239
	s_nop 0
	v_mul_f32_e32 v239, 0x3f666666, v239
	v_min_f32_e32 v240, v239, v240
	v_max_f32_e32 v239, 0x3e4ccccd, v239
	v_cndmask_b32_e64 v239, v240, v239, s[2:3]
	v_mul_f32_e32 v1, v241, v239
	s_mov_b64 s[22:23], s[2:3]
	s_branch .Lrk_top

	.amdhsa_kernel _Z10ode_kernelPKfPKDF16_S2_PfPKi
		.amdhsa_group_segment_fixed_size 148624
		.amdhsa_private_segment_fixed_size 0
		.amdhsa_kernarg_size 40
		.amdhsa_user_sgpr_count 2
		.amdhsa_user_sgpr_dispatch_ptr 0
		.amdhsa_user_sgpr_queue_ptr 0
		.amdhsa_user_sgpr_kernarg_segment_ptr 1
		.amdhsa_user_sgpr_dispatch_id 0
		.amdhsa_user_sgpr_kernarg_preload_length 0
		.amdhsa_user_sgpr_kernarg_preload_offset 0
		.amdhsa_user_sgpr_private_segment_size 0
		.amdhsa_uses_dynamic_stack 0
		.amdhsa_enable_private_segment 0
		.amdhsa_system_sgpr_workgroup_id_x 1
		.amdhsa_system_sgpr_workgroup_id_y 0
		.amdhsa_system_sgpr_workgroup_id_z 0
		.amdhsa_system_sgpr_workgroup_info 0
		.amdhsa_system_vgpr_workitem_id 0
		.amdhsa_next_free_vgpr 512
		.amdhsa_next_free_sgpr 96
		.amdhsa_accum_offset 256
		.amdhsa_reserve_vcc 1
		.amdhsa_float_round_mode_32 0
		.amdhsa_float_round_mode_16_64 0
		.amdhsa_float_denorm_mode_32 3
		.amdhsa_float_denorm_mode_16_64 3
		.amdhsa_dx10_clamp 1
		.amdhsa_ieee_mode 1
		.amdhsa_fp16_overflow 0
		.amdhsa_tg_split 0
		.amdhsa_exception_fp_ieee_invalid_op 0
		.amdhsa_exception_fp_denorm_src 0
		.amdhsa_exception_fp_ieee_div_zero 0
		.amdhsa_exception_fp_ieee_overflow 0
		.amdhsa_exception_fp_ieee_underflow 0
		.amdhsa_exception_fp_ieee_inexact 0
		.amdhsa_exception_int_div_zero 0
	.end_amdhsa_kernel

amdhsa.kernels:
  - .agpr_count:     0
    .args:
      - .actual_access:  read_only
        .address_space:  global
        .offset:         0
        .size:           8
        .value_kind:     global_buffer
      - .actual_access:  read_only
        .address_space:  global
        .offset:         8
        .size:           8
        .value_kind:     global_buffer
      - .actual_access:  read_only
        .address_space:  global
        .offset:         16
        .size:           8
        .value_kind:     global_buffer
      - .actual_access:  write_only
        .address_space:  global
        .offset:         24
        .size:           8
        .value_kind:     global_buffer
      - .actual_access:  write_only
        .address_space:  global
        .offset:         32
        .size:           8
        .value_kind:     global_buffer
      - .actual_access:  write_only
        .address_space:  global
        .offset:         40
        .size:           8
        .value_kind:     global_buffer
      - .actual_access:  read_only
        .address_space:  global
        .offset:         48
        .size:           8
        .value_kind:     global_buffer
      - .actual_access:  write_only
        .address_space:  global
        .offset:         56
        .size:           8
        .value_kind:     global_buffer
    .group_segment_fixed_size: 24576
    .kernarg_segment_align: 8
    .kernarg_segment_size: 64
    .language:       OpenCL C
    .language_version:
      - 2
      - 0
    .max_flat_workgroup_size: 512
    .name:           _Z11prep_kernelPKfS0_S0_PDF16_PfPiS0_S1_
    .private_segment_fixed_size: 0
    .sgpr_count:     102
    .sgpr_spill_count: 0
    .symbol:         _Z11prep_kernelPKfS0_S0_PDF16_PfPiS0_S1_.kd
    .uniform_work_group_size: 1
    .uses_dynamic_stack: false
    .vgpr_count:     160
    .vgpr_spill_count: 0
    .wavefront_size: 64
  - .agpr_count:     256
    .args:
      - .actual_access:  read_only
        .address_space:  global
        .offset:         0
        .size:           8
        .value_kind:     global_buffer
      - .actual_access:  read_only
        .address_space:  global
        .offset:         8
        .size:           8
        .value_kind:     global_buffer
      - .actual_access:  read_only
        .address_space:  global
        .offset:         16
        .size:           8
        .value_kind:     global_buffer
      - .actual_access:  write_only
        .address_space:  global
        .offset:         24
        .size:           8
        .value_kind:     global_buffer
      - .actual_access:  read_only
        .address_space:  global
        .offset:         32
        .size:           8
        .value_kind:     global_buffer
    .group_segment_fixed_size: 148624
    .kernarg_segment_align: 8
    .kernarg_segment_size: 40
    .language:       OpenCL C
    .language_version:
      - 2
      - 0
    .max_flat_workgroup_size: 256
    .name:           _Z10ode_kernelPKfPKDF16_S2_PfPKi
    .private_segment_fixed_size: 0
    .sgpr_count:     49
    .sgpr_spill_count: 0
    .symbol:         _Z10ode_kernelPKfPKDF16_S2_PfPKi.kd
    .uniform_work_group_size: 1
    .uses_dynamic_stack: false
    .vgpr_count:     512
    .vgpr_spill_count: 0
    .wavefront_size: 64
